# MoE GEMM1 epilogue: lin clamp via clamp modifier on packed FMA (2 fewer VALU per pair)
# baseline (speedup 1.0000x reference)
; template <class Epi, class Src>
; __device__ __forceinline__ void gemm_phase(LAS unsigned char* lds, const Src S, const Epi E) {
;     ...
;         for (int t = 0; t < NKTR - 2; t += 2) {
;             const size_t k1 = (size_t)(t + 1) * kstep, k2 = (size_t)(t + 2) * kstep;
;             const char* b2 = cB + k2; const char* b3 = b2 + kstep;
;             G8_ITER(cA, par, k1, cA, par, k2, b2, b3);
.LBB0_1369:
	s_ashr_i32 s27, s26, 31
	s_lshl_b64 s[0:1], s[26:27], 18
	s_lshl_b64 s[2:3], s[22:23], 21
	s_add_u32 s2, s40, s2
	s_addc_u32 s3, s41, s3
	s_add_u32 s28, s2, s0
	v_lshl_add_u32 v134, s68, 10, v156
	s_addc_u32 s29, s3, s1
	s_and_b64 s[0:1], s[24:25], exec
	s_cselect_b32 s1, s29, s21
	s_cselect_b32 s0, s28, s20
	s_add_u32 s2, s20, 0x100
	s_addc_u32 s3, s21, 0
	v_add_u32_e32 v132, s43, v157
	s_mov_b64 s[94:95], 0x80
	s_add_i32 s23, s47, 0xc000
	s_add_i32 s17, s47, 0xe000
	ds_read_b128 v[136:139], v132
	ds_read_b128 v[140:143], v132 offset:1024
	ds_read_b128 v[160:163], v132 offset:2048
	ds_read_b128 v[164:167], v132 offset:3072
	ds_read_b128 v[168:171], v158
	ds_read_b128 v[172:175], v158 offset:1024
	ds_read_b128 v[176:179], v158 offset:2048
	ds_read_b128 v[180:183], v158 offset:3072
	ds_read_b128 v[184:187], v158 offset:4096
	ds_read_b128 v[188:191], v158 offset:5120
	ds_read_b128 v[192:195], v158 offset:6144
	ds_read_b128 v[196:199], v158 offset:7168
	s_add_u32 s94, s8, 0x80
	s_addc_u32 s95, s9, 0
	v_and_b32_e32 v34, 0xffff, v255
	v_lshl_add_u32 v34, v34, 10, v155
	s_mov_b32 m0, s23
	s_nop 0
	global_load_lds_dwordx4 v34, s[94:95]
	v_lshrrev_b32_e32 v34, 16, v255
	v_lshl_add_u32 v34, v34, 10, v155
	s_mov_b32 m0, s17
	s_nop 0
	global_load_lds_dwordx4 v34, s[94:95]
	s_waitcnt lgkmcnt(8)
	s_barrier
	s_waitcnt lgkmcnt(0)
	s_setprio 1
	s_waitcnt lgkmcnt(0)
	v_mfma_scale_f32_16x16x128_f8f6f4 v[150:153], v[136:143], v[168:175], 0, v154, v154 op_sel_hi:[0,0,0]
	v_mfma_scale_f32_16x16x128_f8f6f4 v[208:211], v[160:167], v[168:175], 0, v154, v154 op_sel_hi:[0,0,0]
	v_mfma_scale_f32_16x16x128_f8f6f4 v[212:215], v[136:143], v[176:183], 0, v154, v154 op_sel_hi:[0,0,0]
	v_mfma_scale_f32_16x16x128_f8f6f4 v[216:219], v[160:167], v[176:183], 0, v154, v154 op_sel_hi:[0,0,0]
	v_mfma_scale_f32_16x16x128_f8f6f4 v[220:223], v[136:143], v[184:191], 0, v154, v154 op_sel_hi:[0,0,0]
	v_mfma_scale_f32_16x16x128_f8f6f4 v[224:227], v[160:167], v[184:191], 0, v154, v154 op_sel_hi:[0,0,0]
	v_mfma_scale_f32_16x16x128_f8f6f4 v[228:231], v[136:143], v[192:199], 0, v154, v154 op_sel_hi:[0,0,0]
	v_mfma_scale_f32_16x16x128_f8f6f4 v[232:235], v[160:167], v[192:199], 0, v154, v154 op_sel_hi:[0,0,0]
	s_setprio 0
	s_barrier
	s_add_u32 s74, s20, 0x10100
	v_add_u32_e32 v133, s49, v157
	s_addc_u32 s75, s21, 0
	s_mov_b32 m0, s44
	ds_read_b128 v[124:127], v133
	ds_read_b128 v[128:131], v133 offset:1024
	ds_read_b128 v[200:203], v133 offset:2048
	ds_read_b128 v[204:207], v133 offset:3072
	s_nop 0
	v_lshl_add_u64 v[68:69], s[2:3], 0, v[252:253]
	global_load_lds_dwordx4 v[68:69], off
	v_lshl_add_u64 v[68:69], s[74:75], 0, v[252:253]
	s_mov_b32 m0, s45
	s_nop 0
	global_load_lds_dwordx4 v[68:69], off
	s_barrier
	s_waitcnt lgkmcnt(0)
	s_setprio 1
	s_waitcnt lgkmcnt(0)
	v_mfma_scale_f32_16x16x128_f8f6f4 v[96:99], v[124:131], v[168:175], 0, v154, v154 op_sel_hi:[0,0,0]
	v_mfma_scale_f32_16x16x128_f8f6f4 v[92:95], v[200:207], v[168:175], 0, v154, v154 op_sel_hi:[0,0,0]
	v_mfma_scale_f32_16x16x128_f8f6f4 v[88:91], v[124:131], v[176:183], 0, v154, v154 op_sel_hi:[0,0,0]
	v_mfma_scale_f32_16x16x128_f8f6f4 v[84:87], v[200:207], v[176:183], 0, v154, v154 op_sel_hi:[0,0,0]
	v_mfma_scale_f32_16x16x128_f8f6f4 v[80:83], v[124:131], v[184:191], 0, v154, v154 op_sel_hi:[0,0,0]
	v_mfma_scale_f32_16x16x128_f8f6f4 v[76:79], v[200:207], v[184:191], 0, v154, v154 op_sel_hi:[0,0,0]
	v_mfma_scale_f32_16x16x128_f8f6f4 v[72:75], v[124:131], v[192:199], 0, v154, v154 op_sel_hi:[0,0,0]
	v_mfma_scale_f32_16x16x128_f8f6f4 v[68:71], v[200:207], v[192:199], 0, v154, v154 op_sel_hi:[0,0,0]
	s_setprio 0
	s_barrier
	s_nop 0
	s_mov_b64 s[76:77], 0x100
	ds_read_b128 v[104:107], v158 offset:16384
	ds_read_b128 v[108:111], v158 offset:17408
	ds_read_b128 v[112:115], v158 offset:18432
	ds_read_b128 v[116:119], v158 offset:19456
	ds_read_b128 v[168:171], v158 offset:20480
	ds_read_b128 v[172:175], v158 offset:21504
	ds_read_b128 v[176:179], v158 offset:22528
	ds_read_b128 v[180:183], v158 offset:23552
	s_add_u32 s94, s8, 0x100
	s_addc_u32 s95, s9, 0
	v_and_b32_e32 v34, 0xffff, v159
	v_lshl_add_u32 v34, v34, 10, v155
	s_mov_b32 m0, s47
	s_nop 0
	global_load_lds_dwordx4 v34, s[94:95]
	v_lshrrev_b32_e32 v34, 16, v159
	v_lshl_add_u32 v34, v34, 10, v155
	s_mov_b32 m0, s48
	s_nop 0
	global_load_lds_dwordx4 v34, s[94:95]
	s_barrier
	s_waitcnt lgkmcnt(0)
	s_setprio 1
	s_waitcnt lgkmcnt(0)
	v_mfma_scale_f32_16x16x128_f8f6f4 v[64:67], v[136:143], v[104:111], 0, v154, v154 op_sel_hi:[0,0,0]
	v_mfma_scale_f32_16x16x128_f8f6f4 v[60:63], v[160:167], v[104:111], 0, v154, v154 op_sel_hi:[0,0,0]
	v_mfma_scale_f32_16x16x128_f8f6f4 v[56:59], v[136:143], v[112:119], 0, v154, v154 op_sel_hi:[0,0,0]
	v_mfma_scale_f32_16x16x128_f8f6f4 v[52:55], v[160:167], v[112:119], 0, v154, v154 op_sel_hi:[0,0,0]
	v_mfma_scale_f32_16x16x128_f8f6f4 v[48:51], v[136:143], v[168:175], 0, v154, v154 op_sel_hi:[0,0,0]
	v_mfma_scale_f32_16x16x128_f8f6f4 v[44:47], v[160:167], v[168:175], 0, v154, v154 op_sel_hi:[0,0,0]
	v_mfma_scale_f32_16x16x128_f8f6f4 v[40:43], v[136:143], v[176:183], 0, v154, v154 op_sel_hi:[0,0,0]
	v_mfma_scale_f32_16x16x128_f8f6f4 v[36:39], v[160:167], v[176:183], 0, v154, v154 op_sel_hi:[0,0,0]
	s_setprio 0
	s_barrier
	s_add_u32 s2, s20, 0x20100
	s_addc_u32 s3, s21, 0
	s_add_u32 s74, s20, 0x30100
	s_addc_u32 s75, s21, 0
	s_mov_b32 m0, s50
	s_nop 0
	v_lshl_add_u64 v[6:7], s[2:3], 0, v[252:253]
	global_load_lds_dwordx4 v[6:7], off
	v_lshl_add_u64 v[6:7], s[74:75], 0, v[252:253]
	s_mov_b32 m0, s51
	s_nop 0
	global_load_lds_dwordx4 v[6:7], off
	s_waitcnt vmcnt(6)
	s_barrier
	s_setprio 1
	v_mfma_scale_f32_16x16x128_f8f6f4 v[100:103], v[124:131], v[104:111], 0, v154, v154 op_sel_hi:[0,0,0]
	v_mfma_scale_f32_16x16x128_f8f6f4 v[104:107], v[200:207], v[104:111], 0, v154, v154 op_sel_hi:[0,0,0]
	v_mfma_scale_f32_16x16x128_f8f6f4 v[108:111], v[124:131], v[112:119], 0, v154, v154 op_sel_hi:[0,0,0]
	v_mfma_scale_f32_16x16x128_f8f6f4 v[112:115], v[200:207], v[112:119], 0, v154, v154 op_sel_hi:[0,0,0]
	v_mfma_scale_f32_16x16x128_f8f6f4 v[116:119], v[124:131], v[168:175], 0, v154, v154 op_sel_hi:[0,0,0]
	v_mfma_scale_f32_16x16x128_f8f6f4 v[120:123], v[200:207], v[168:175], 0, v154, v154 op_sel_hi:[0,0,0]
	v_mfma_scale_f32_16x16x128_f8f6f4 v[124:127], v[124:131], v[176:183], 0, v154, v154 op_sel_hi:[0,0,0]
	v_mfma_scale_f32_16x16x128_f8f6f4 v[128:131], v[200:207], v[176:183], 0, v154, v154 op_sel_hi:[0,0,0]
	s_setprio 0
	s_barrier
	s_nop 4
	v_add_u32_e32 v135, s58, v157
	ds_read_b128 v[138:141], v135
	ds_read_b128 v[142:145], v135 offset:1024
	ds_read_b128 v[160:163], v135 offset:2048
	ds_read_b128 v[164:167], v135 offset:3072
	ds_read_b128 v[168:171], v158 offset:32768
	ds_read_b128 v[172:175], v158 offset:33792
	ds_read_b128 v[176:179], v158 offset:34816
	ds_read_b128 v[180:183], v158 offset:35840
	ds_read_b128 v[184:187], v158 offset:36864
	ds_read_b128 v[188:191], v158 offset:37888
	ds_read_b128 v[192:195], v158 offset:38912
	ds_read_b128 v[196:199], v158 offset:39936
	s_add_u32 s94, s8, 0x100
	s_addc_u32 s95, s9, 0
	v_and_b32_e32 v34, 0xffff, v255
	v_lshl_add_u32 v34, v34, 10, v155
	s_mov_b32 m0, s52
	s_nop 0
	global_load_lds_dwordx4 v34, s[94:95]
	v_lshrrev_b32_e32 v34, 16, v255
	v_lshl_add_u32 v34, v34, 10, v155
	s_mov_b32 m0, s53
	s_nop 0
	global_load_lds_dwordx4 v34, s[94:95]
	s_waitcnt lgkmcnt(8)
	s_barrier
	s_waitcnt lgkmcnt(0)
	s_setprio 1
	s_waitcnt lgkmcnt(0)
	v_mfma_scale_f32_16x16x128_f8f6f4 v[2:5], v[138:145], v[168:175], v[150:153], v154, v154 op_sel_hi:[0,0,0]
	v_mfma_scale_f32_16x16x128_f8f6f4 v[6:9], v[160:167], v[168:175], v[208:211], v154, v154 op_sel_hi:[0,0,0]
	v_mfma_scale_f32_16x16x128_f8f6f4 v[10:13], v[138:145], v[176:183], v[212:215], v154, v154 op_sel_hi:[0,0,0]
	v_mfma_scale_f32_16x16x128_f8f6f4 v[14:17], v[160:167], v[176:183], v[216:219], v154, v154 op_sel_hi:[0,0,0]
	v_mfma_scale_f32_16x16x128_f8f6f4 v[18:21], v[138:145], v[184:191], v[220:223], v154, v154 op_sel_hi:[0,0,0]
	v_mfma_scale_f32_16x16x128_f8f6f4 v[22:25], v[160:167], v[184:191], v[224:227], v154, v154 op_sel_hi:[0,0,0]
	v_mfma_scale_f32_16x16x128_f8f6f4 v[26:29], v[138:145], v[192:199], v[228:231], v154, v154 op_sel_hi:[0,0,0]
	v_mfma_scale_f32_16x16x128_f8f6f4 v[30:33], v[160:167], v[192:199], v[232:235], v154, v154 op_sel_hi:[0,0,0]
	s_setprio 0
	s_barrier
	s_add_u32 s2, s20, 0x180
	s_addc_u32 s3, s21, 0
	s_add_u32 s74, s20, 0x10180
	v_add_u32_e32 v136, s63, v157
	s_addc_u32 s75, s21, 0
	s_mov_b32 m0, s59
	ds_read_b128 v[200:203], v136
	ds_read_b128 v[204:207], v136 offset:1024
	ds_read_b128 v[208:211], v136 offset:2048
	ds_read_b128 v[212:215], v136 offset:3072
	s_nop 0
	v_lshl_add_u64 v[146:147], s[2:3], 0, v[252:253]
	global_load_lds_dwordx4 v[146:147], off
	v_lshl_add_u64 v[146:147], s[74:75], 0, v[252:253]
	s_mov_b32 m0, s60
	s_nop 0
	global_load_lds_dwordx4 v[146:147], off
	s_barrier
	s_waitcnt lgkmcnt(0)
	s_setprio 1
	s_waitcnt lgkmcnt(0)
	v_mfma_scale_f32_16x16x128_f8f6f4 v[96:99], v[200:207], v[168:175], v[96:99], v154, v154 op_sel_hi:[0,0,0]
	v_mfma_scale_f32_16x16x128_f8f6f4 v[92:95], v[208:215], v[168:175], v[92:95], v154, v154 op_sel_hi:[0,0,0]
	v_mfma_scale_f32_16x16x128_f8f6f4 v[88:91], v[200:207], v[176:183], v[88:91], v154, v154 op_sel_hi:[0,0,0]
	v_mfma_scale_f32_16x16x128_f8f6f4 v[84:87], v[208:215], v[176:183], v[84:87], v154, v154 op_sel_hi:[0,0,0]
	v_mfma_scale_f32_16x16x128_f8f6f4 v[80:83], v[200:207], v[184:191], v[80:83], v154, v154 op_sel_hi:[0,0,0]
	v_mfma_scale_f32_16x16x128_f8f6f4 v[76:79], v[208:215], v[184:191], v[76:79], v154, v154 op_sel_hi:[0,0,0]
	v_mfma_scale_f32_16x16x128_f8f6f4 v[72:75], v[200:207], v[192:199], v[72:75], v154, v154 op_sel_hi:[0,0,0]
	v_mfma_scale_f32_16x16x128_f8f6f4 v[68:71], v[208:215], v[192:199], v[68:71], v154, v154 op_sel_hi:[0,0,0]
	s_setprio 0
	s_barrier
	s_mov_b64 s[76:77], 0x180
	ds_read_b128 v[168:171], v158 offset:49152
	ds_read_b128 v[172:175], v158 offset:50176
	ds_read_b128 v[176:179], v158 offset:51200
	ds_read_b128 v[180:183], v158 offset:52224
	ds_read_b128 v[184:187], v158 offset:53248
	ds_read_b128 v[188:191], v158 offset:54272
	ds_read_b128 v[192:195], v158 offset:55296
	ds_read_b128 v[196:199], v158 offset:56320
	s_add_u32 s94, s8, 0x180
	s_addc_u32 s95, s9, 0
	v_and_b32_e32 v34, 0xffff, v159
	v_lshl_add_u32 v34, v34, 10, v155
	s_mov_b32 m0, s61
	s_nop 0
	global_load_lds_dwordx4 v34, s[94:95]
	v_lshrrev_b32_e32 v34, 16, v159
	v_lshl_add_u32 v34, v34, 10, v155
	s_mov_b32 m0, s62
	s_nop 0
	global_load_lds_dwordx4 v34, s[94:95]
	s_barrier
	s_waitcnt lgkmcnt(0)
	s_setprio 1
	s_waitcnt lgkmcnt(0)
	v_mfma_scale_f32_16x16x128_f8f6f4 v[64:67], v[138:145], v[168:175], v[64:67], v154, v154 op_sel_hi:[0,0,0]
	v_mfma_scale_f32_16x16x128_f8f6f4 v[60:63], v[160:167], v[168:175], v[60:63], v154, v154 op_sel_hi:[0,0,0]
	v_mfma_scale_f32_16x16x128_f8f6f4 v[56:59], v[138:145], v[176:183], v[56:59], v154, v154 op_sel_hi:[0,0,0]
	v_mfma_scale_f32_16x16x128_f8f6f4 v[52:55], v[160:167], v[176:183], v[52:55], v154, v154 op_sel_hi:[0,0,0]
	v_mfma_scale_f32_16x16x128_f8f6f4 v[48:51], v[138:145], v[184:191], v[48:51], v154, v154 op_sel_hi:[0,0,0]
	v_mfma_scale_f32_16x16x128_f8f6f4 v[44:47], v[160:167], v[184:191], v[44:47], v154, v154 op_sel_hi:[0,0,0]
	v_mfma_scale_f32_16x16x128_f8f6f4 v[40:43], v[138:145], v[192:199], v[40:43], v154, v154 op_sel_hi:[0,0,0]
	v_mfma_scale_f32_16x16x128_f8f6f4 v[36:39], v[160:167], v[192:199], v[36:39], v154, v154 op_sel_hi:[0,0,0]
	s_setprio 0
	s_barrier
	s_add_u32 s2, s20, 0x20180
	s_addc_u32 s3, s21, 0
	s_add_u32 s74, s20, 0x30180
	s_addc_u32 s75, s21, 0
	s_mov_b32 m0, s64
	s_nop 0
	v_lshl_add_u64 v[138:139], s[2:3], 0, v[252:253]
	global_load_lds_dwordx4 v[138:139], off
	v_lshl_add_u64 v[138:139], s[74:75], 0, v[252:253]
	s_mov_b32 m0, s65
	s_nop 0
	global_load_lds_dwordx4 v[138:139], off
	s_waitcnt vmcnt(6)
	s_barrier
	s_setprio 1
	v_mfma_scale_f32_16x16x128_f8f6f4 v[108:111], v[200:207], v[176:183], v[108:111], v154, v154 op_sel_hi:[0,0,0]
	v_mfma_scale_f32_16x16x128_f8f6f4 v[112:115], v[208:215], v[176:183], v[112:115], v154, v154 op_sel_hi:[0,0,0]
	v_mfma_scale_f32_16x16x128_f8f6f4 v[116:119], v[200:207], v[184:191], v[116:119], v154, v154 op_sel_hi:[0,0,0]
	v_mfma_scale_f32_16x16x128_f8f6f4 v[120:123], v[208:215], v[184:191], v[120:123], v154, v154 op_sel_hi:[0,0,0]
	v_mfma_scale_f32_16x16x128_f8f6f4 v[124:127], v[200:207], v[192:199], v[124:127], v154, v154 op_sel_hi:[0,0,0]
	v_mfma_scale_f32_16x16x128_f8f6f4 v[128:131], v[208:215], v[192:199], v[128:131], v154, v154 op_sel_hi:[0,0,0]
	v_mfma_scale_f32_16x16x128_f8f6f4 v[100:103], v[200:207], v[168:175], v[100:103], v154, v154 op_sel_hi:[0,0,0]
	v_mfma_scale_f32_16x16x128_f8f6f4 v[104:107], v[208:215], v[168:175], v[104:107], v154, v154 op_sel_hi:[0,0,0]
	s_setprio 0
	s_barrier
	s_add_u32 s2, s20, 0x200
	s_addc_u32 s3, s21, 0
	ds_read_b128 v[138:141], v132
	ds_read_b128 v[142:145], v132 offset:1024
	ds_read_b128 v[160:163], v132 offset:2048
	ds_read_b128 v[164:167], v132 offset:3072
	ds_read_b128 v[168:171], v158
	ds_read_b128 v[172:175], v158 offset:1024
	ds_read_b128 v[176:179], v158 offset:2048
	ds_read_b128 v[180:183], v158 offset:3072
	ds_read_b128 v[184:187], v158 offset:4096
	ds_read_b128 v[188:191], v158 offset:5120
	ds_read_b128 v[192:195], v158 offset:6144
	ds_read_b128 v[196:199], v158 offset:7168
	s_add_u32 s94, s8, 0x180
	s_addc_u32 s95, s9, 0
	v_and_b32_e32 v34, 0xffff, v255
	v_lshl_add_u32 v34, v34, 10, v155
	s_mov_b32 m0, s23
	s_nop 0
	global_load_lds_dwordx4 v34, s[94:95]
	v_lshrrev_b32_e32 v34, 16, v255
	v_lshl_add_u32 v34, v34, 10, v155
	s_mov_b32 m0, s17
	s_nop 0
	global_load_lds_dwordx4 v34, s[94:95]
	s_waitcnt lgkmcnt(8)
	s_barrier
	s_waitcnt lgkmcnt(0)
	s_setprio 1
	s_waitcnt lgkmcnt(0)
	v_mfma_scale_f32_16x16x128_f8f6f4 v[204:207], v[138:145], v[176:183], v[10:13], v154, v154 op_sel_hi:[0,0,0]
	v_mfma_scale_f32_16x16x128_f8f6f4 v[150:153], v[138:145], v[168:175], v[2:5], v154, v154 op_sel_hi:[0,0,0]
	v_mfma_scale_f32_16x16x128_f8f6f4 v[200:203], v[160:167], v[168:175], v[6:9], v154, v154 op_sel_hi:[0,0,0]
	v_mfma_scale_f32_16x16x128_f8f6f4 v[208:211], v[160:167], v[176:183], v[14:17], v154, v154 op_sel_hi:[0,0,0]
	v_mfma_scale_f32_16x16x128_f8f6f4 v[212:215], v[138:145], v[184:191], v[18:21], v154, v154 op_sel_hi:[0,0,0]
	v_mfma_scale_f32_16x16x128_f8f6f4 v[216:219], v[160:167], v[184:191], v[22:25], v154, v154 op_sel_hi:[0,0,0]
	v_mfma_scale_f32_16x16x128_f8f6f4 v[220:223], v[138:145], v[192:199], v[26:29], v154, v154 op_sel_hi:[0,0,0]
	v_mfma_scale_f32_16x16x128_f8f6f4 v[224:227], v[160:167], v[192:199], v[30:33], v154, v154 op_sel_hi:[0,0,0]
	s_setprio 0
	s_barrier
	s_add_u32 s74, s20, 0x10200
	s_addc_u32 s75, s21, 0
	s_mov_b32 m0, s44
	ds_read_b128 v[2:5], v133
	ds_read_b128 v[6:9], v133 offset:1024
	ds_read_b128 v[10:13], v133 offset:2048
	ds_read_b128 v[14:17], v133 offset:3072
	s_nop 0
	v_lshl_add_u64 v[18:19], s[2:3], 0, v[252:253]
	global_load_lds_dwordx4 v[18:19], off
	v_lshl_add_u64 v[18:19], s[74:75], 0, v[252:253]
	s_mov_b32 m0, s45
	s_nop 0
	global_load_lds_dwordx4 v[18:19], off
	s_barrier
	s_waitcnt lgkmcnt(0)
	s_setprio 1
	s_waitcnt lgkmcnt(0)
	v_mfma_scale_f32_16x16x128_f8f6f4 v[88:91], v[2:9], v[176:183], v[88:91], v154, v154 op_sel_hi:[0,0,0]
	v_mfma_scale_f32_16x16x128_f8f6f4 v[84:87], v[10:17], v[176:183], v[84:87], v154, v154 op_sel_hi:[0,0,0]
	v_mfma_scale_f32_16x16x128_f8f6f4 v[228:231], v[2:9], v[168:175], v[96:99], v154, v154 op_sel_hi:[0,0,0]
	v_mfma_scale_f32_16x16x128_f8f6f4 v[168:171], v[10:17], v[168:175], v[92:95], v154, v154 op_sel_hi:[0,0,0]
	v_mfma_scale_f32_16x16x128_f8f6f4 v[172:175], v[2:9], v[184:191], v[80:83], v154, v154 op_sel_hi:[0,0,0]
	v_mfma_scale_f32_16x16x128_f8f6f4 v[176:179], v[10:17], v[184:191], v[76:79], v154, v154 op_sel_hi:[0,0,0]
	v_mfma_scale_f32_16x16x128_f8f6f4 v[180:183], v[2:9], v[192:199], v[72:75], v154, v154 op_sel_hi:[0,0,0]
	v_mfma_scale_f32_16x16x128_f8f6f4 v[184:187], v[10:17], v[192:199], v[68:71], v154, v154 op_sel_hi:[0,0,0]
	s_setprio 0
	s_barrier
	s_nop 0
	s_mov_b64 s[76:77], 0x200
	ds_read_b128 v[18:21], v158 offset:16384
	ds_read_b128 v[22:25], v158 offset:17408
	ds_read_b128 v[26:29], v158 offset:18432
	ds_read_b128 v[30:33], v158 offset:19456
	ds_read_b128 v[68:71], v158 offset:20480
	ds_read_b128 v[72:75], v158 offset:21504
	ds_read_b128 v[76:79], v158 offset:22528
	ds_read_b128 v[80:83], v158 offset:23552
	s_add_u32 s94, s8, 0x200
	s_addc_u32 s95, s9, 0
	v_and_b32_e32 v34, 0xffff, v159
	v_lshl_add_u32 v34, v34, 10, v155
	s_mov_b32 m0, s47
	s_nop 0
	global_load_lds_dwordx4 v34, s[94:95]
	v_lshrrev_b32_e32 v34, 16, v159
	v_lshl_add_u32 v34, v34, 10, v155
	s_mov_b32 m0, s48
	s_nop 0
	global_load_lds_dwordx4 v34, s[94:95]
	s_barrier
	s_waitcnt lgkmcnt(0)
	s_setprio 1
	s_waitcnt lgkmcnt(0)
	v_mfma_scale_f32_16x16x128_f8f6f4 v[236:239], v[138:145], v[68:75], v[48:51], v154, v154 op_sel_hi:[0,0,0]
	v_mfma_scale_f32_16x16x128_f8f6f4 v[240:243], v[160:167], v[68:75], v[44:47], v154, v154 op_sel_hi:[0,0,0]
	v_mfma_scale_f32_16x16x128_f8f6f4 v[244:247], v[138:145], v[76:83], v[40:43], v154, v154 op_sel_hi:[0,0,0]
	v_mfma_scale_f32_16x16x128_f8f6f4 v[248:251], v[160:167], v[76:83], v[36:39], v154, v154 op_sel_hi:[0,0,0]
	v_mfma_scale_f32_16x16x128_f8f6f4 v[188:191], v[138:145], v[18:25], v[64:67], v154, v154 op_sel_hi:[0,0,0]
	v_mfma_scale_f32_16x16x128_f8f6f4 v[192:195], v[160:167], v[18:25], v[60:63], v154, v154 op_sel_hi:[0,0,0]
	v_mfma_scale_f32_16x16x128_f8f6f4 v[196:199], v[138:145], v[26:33], v[56:59], v154, v154 op_sel_hi:[0,0,0]
	v_mfma_scale_f32_16x16x128_f8f6f4 v[232:235], v[160:167], v[26:33], v[52:55], v154, v154 op_sel_hi:[0,0,0]
	s_setprio 0
	s_barrier
	s_add_u32 s2, s20, 0x20200
	s_addc_u32 s3, s21, 0
	s_add_u32 s74, s20, 0x30200
	s_addc_u32 s75, s21, 0
	s_mov_b32 m0, s50
	s_nop 0
	v_lshl_add_u64 v[36:37], s[2:3], 0, v[252:253]
	global_load_lds_dwordx4 v[36:37], off
	v_lshl_add_u64 v[36:37], s[74:75], 0, v[252:253]
	s_mov_b32 m0, s51
	s_nop 0
	global_load_lds_dwordx4 v[36:37], off
	s_waitcnt vmcnt(6)
	s_barrier
	s_setprio 1
	v_mfma_scale_f32_16x16x128_f8f6f4 v[146:149], v[2:9], v[18:25], v[100:103], v154, v154 op_sel_hi:[0,0,0]
	v_mfma_scale_f32_16x16x128_f8f6f4 v[18:21], v[10:17], v[18:25], v[104:107], v154, v154 op_sel_hi:[0,0,0]
	v_mfma_scale_f32_16x16x128_f8f6f4 v[22:25], v[2:9], v[26:33], v[108:111], v154, v154 op_sel_hi:[0,0,0]
	v_mfma_scale_f32_16x16x128_f8f6f4 v[26:29], v[10:17], v[26:33], v[112:115], v154, v154 op_sel_hi:[0,0,0]
	v_mfma_scale_f32_16x16x128_f8f6f4 v[30:33], v[2:9], v[68:75], v[116:119], v154, v154 op_sel_hi:[0,0,0]
	v_mfma_scale_f32_16x16x128_f8f6f4 v[36:39], v[10:17], v[68:75], v[120:123], v154, v154 op_sel_hi:[0,0,0]
	v_mfma_scale_f32_16x16x128_f8f6f4 v[72:75], v[2:9], v[76:83], v[124:127], v154, v154 op_sel_hi:[0,0,0]
	v_mfma_scale_f32_16x16x128_f8f6f4 v[76:79], v[10:17], v[76:83], v[128:131], v154, v154 op_sel_hi:[0,0,0]
	s_setprio 0
	s_barrier
	ds_read_b128 v[92:95], v135
	ds_read_b128 v[96:99], v135 offset:1024
	ds_read_b128 v[100:103], v135 offset:2048
	ds_read_b128 v[104:107], v135 offset:3072
	ds_read_b128 v[40:43], v158 offset:32768
	ds_read_b128 v[44:47], v158 offset:33792
	ds_read_b128 v[48:51], v158 offset:34816
	ds_read_b128 v[52:55], v158 offset:35840
	ds_read_b128 v[56:59], v158 offset:36864
	ds_read_b128 v[60:63], v158 offset:37888
	ds_read_b128 v[64:67], v158 offset:38912
	ds_read_b128 v[68:71], v158 offset:39936
	s_add_u32 s94, s8, 0x200
	s_addc_u32 s95, s9, 0
	v_and_b32_e32 v34, 0xffff, v255
	v_lshl_add_u32 v34, v34, 10, v155
	s_mov_b32 m0, s52
	s_nop 0
	global_load_lds_dwordx4 v34, s[94:95]
	v_lshrrev_b32_e32 v34, 16, v255
	v_lshl_add_u32 v34, v34, 10, v155
	s_mov_b32 m0, s53
	s_nop 0
	global_load_lds_dwordx4 v34, s[94:95]
	s_waitcnt lgkmcnt(8)
	s_barrier
	s_waitcnt lgkmcnt(0)
	s_setprio 1
	s_waitcnt lgkmcnt(0)
	v_mfma_scale_f32_16x16x128_f8f6f4 v[2:5], v[92:99], v[40:47], v[150:153], v154, v154 op_sel_hi:[0,0,0]
	v_mfma_scale_f32_16x16x128_f8f6f4 v[6:9], v[100:107], v[40:47], v[200:203], v154, v154 op_sel_hi:[0,0,0]
	v_mfma_scale_f32_16x16x128_f8f6f4 v[10:13], v[92:99], v[48:55], v[204:207], v154, v154 op_sel_hi:[0,0,0]
	v_mfma_scale_f32_16x16x128_f8f6f4 v[14:17], v[100:107], v[48:55], v[208:211], v154, v154 op_sel_hi:[0,0,0]
	v_mfma_scale_f32_16x16x128_f8f6f4 v[204:207], v[92:99], v[64:71], v[220:223], v154, v154 op_sel_hi:[0,0,0]
	v_mfma_scale_f32_16x16x128_f8f6f4 v[150:153], v[92:99], v[56:63], v[212:215], v154, v154 op_sel_hi:[0,0,0]
	v_mfma_scale_f32_16x16x128_f8f6f4 v[200:203], v[100:107], v[56:63], v[216:219], v154, v154 op_sel_hi:[0,0,0]
	v_mfma_scale_f32_16x16x128_f8f6f4 v[208:211], v[100:107], v[64:71], v[224:227], v154, v154 op_sel_hi:[0,0,0]
	s_setprio 0
	s_barrier
	s_add_u32 s2, s20, 0x280
	s_addc_u32 s3, s21, 0
	s_add_u32 s74, s20, 0x10280
	s_addc_u32 s75, s21, 0
	s_mov_b32 m0, s59
	ds_read_b128 v[124:127], v136
	ds_read_b128 v[128:131], v136 offset:1024
	ds_read_b128 v[138:141], v136 offset:2048
	ds_read_b128 v[142:145], v136 offset:3072
	s_nop 0
	v_lshl_add_u64 v[80:81], s[2:3], 0, v[252:253]
	global_load_lds_dwordx4 v[80:81], off
	v_lshl_add_u64 v[80:81], s[74:75], 0, v[252:253]
	s_mov_b32 m0, s60
	s_nop 0
	global_load_lds_dwordx4 v[80:81], off
	s_barrier
	s_waitcnt lgkmcnt(0)
	s_setprio 1
	s_waitcnt lgkmcnt(0)
	v_mfma_scale_f32_16x16x128_f8f6f4 v[212:215], v[124:131], v[40:47], v[228:231], v154, v154 op_sel_hi:[0,0,0]
	v_mfma_scale_f32_16x16x128_f8f6f4 v[40:43], v[138:145], v[40:47], v[168:171], v154, v154 op_sel_hi:[0,0,0]
	v_mfma_scale_f32_16x16x128_f8f6f4 v[44:47], v[124:131], v[48:55], v[88:91], v154, v154 op_sel_hi:[0,0,0]
	v_mfma_scale_f32_16x16x128_f8f6f4 v[48:51], v[138:145], v[48:55], v[84:87], v154, v154 op_sel_hi:[0,0,0]
	v_mfma_scale_f32_16x16x128_f8f6f4 v[52:55], v[124:131], v[56:63], v[172:175], v154, v154 op_sel_hi:[0,0,0]
	v_mfma_scale_f32_16x16x128_f8f6f4 v[56:59], v[138:145], v[56:63], v[176:179], v154, v154 op_sel_hi:[0,0,0]
	v_mfma_scale_f32_16x16x128_f8f6f4 v[60:63], v[124:131], v[64:71], v[180:183], v154, v154 op_sel_hi:[0,0,0]
	v_mfma_scale_f32_16x16x128_f8f6f4 v[64:67], v[138:145], v[64:71], v[184:187], v154, v154 op_sel_hi:[0,0,0]
	s_setprio 0
	s_barrier
	s_mov_b64 s[76:77], 0x280
	ds_read_b128 v[108:111], v158 offset:49152
	ds_read_b128 v[112:115], v158 offset:50176
	ds_read_b128 v[116:119], v158 offset:51200
	ds_read_b128 v[120:123], v158 offset:52224
	ds_read_b128 v[160:163], v158 offset:53248
	ds_read_b128 v[164:167], v158 offset:54272
	ds_read_b128 v[168:171], v158 offset:55296
	ds_read_b128 v[172:175], v158 offset:56320
	s_add_u32 s94, s8, 0x280
	s_addc_u32 s95, s9, 0
	v_and_b32_e32 v34, 0xffff, v159
	v_lshl_add_u32 v34, v34, 10, v155
	s_mov_b32 m0, s61
	s_nop 0
	global_load_lds_dwordx4 v34, s[94:95]
	v_lshrrev_b32_e32 v34, 16, v159
	v_lshl_add_u32 v34, v34, 10, v155
	s_mov_b32 m0, s62
	s_nop 0
	global_load_lds_dwordx4 v34, s[94:95]
	s_barrier
	s_waitcnt lgkmcnt(0)
	s_setprio 1
	s_waitcnt lgkmcnt(0)
	v_mfma_scale_f32_16x16x128_f8f6f4 v[68:71], v[92:99], v[108:115], v[188:191], v154, v154 op_sel_hi:[0,0,0]
	v_mfma_scale_f32_16x16x128_f8f6f4 v[220:223], v[92:99], v[116:123], v[196:199], v154, v154 op_sel_hi:[0,0,0]
	v_mfma_scale_f32_16x16x128_f8f6f4 v[80:83], v[100:107], v[116:123], v[232:235], v154, v154 op_sel_hi:[0,0,0]
	v_mfma_scale_f32_16x16x128_f8f6f4 v[84:87], v[92:99], v[160:167], v[236:239], v154, v154 op_sel_hi:[0,0,0]
	v_mfma_scale_f32_16x16x128_f8f6f4 v[88:91], v[100:107], v[160:167], v[240:243], v154, v154 op_sel_hi:[0,0,0]
	v_mfma_scale_f32_16x16x128_f8f6f4 v[92:95], v[92:99], v[168:175], v[244:247], v154, v154 op_sel_hi:[0,0,0]
	v_mfma_scale_f32_16x16x128_f8f6f4 v[96:99], v[100:107], v[168:175], v[248:251], v154, v154 op_sel_hi:[0,0,0]
	v_mfma_scale_f32_16x16x128_f8f6f4 v[216:219], v[100:107], v[108:115], v[192:195], v154, v154 op_sel_hi:[0,0,0]
	s_setprio 0
	s_barrier
	s_add_u32 s2, s20, 0x20280
	s_addc_u32 s3, s21, 0
	s_add_u32 s74, s20, 0x30280
	s_addc_u32 s75, s21, 0
	s_mov_b32 m0, s64
	s_nop 0
	v_lshl_add_u64 v[100:101], s[2:3], 0, v[252:253]
	global_load_lds_dwordx4 v[100:101], off
	v_lshl_add_u64 v[100:101], s[74:75], 0, v[252:253]
	s_mov_b32 m0, s65
	s_nop 0
	global_load_lds_dwordx4 v[100:101], off
	s_waitcnt vmcnt(6)
	s_barrier
	s_setprio 1
	v_mfma_scale_f32_16x16x128_f8f6f4 v[100:103], v[124:131], v[108:115], v[146:149], v154, v154 op_sel_hi:[0,0,0]
	v_mfma_scale_f32_16x16x128_f8f6f4 v[104:107], v[138:145], v[108:115], v[18:21], v154, v154 op_sel_hi:[0,0,0]
	v_mfma_scale_f32_16x16x128_f8f6f4 v[108:111], v[124:131], v[116:123], v[22:25], v154, v154 op_sel_hi:[0,0,0]
	v_mfma_scale_f32_16x16x128_f8f6f4 v[112:115], v[138:145], v[116:123], v[26:29], v154, v154 op_sel_hi:[0,0,0]
	v_mfma_scale_f32_16x16x128_f8f6f4 v[116:119], v[124:131], v[160:167], v[30:33], v154, v154 op_sel_hi:[0,0,0]
	v_mfma_scale_f32_16x16x128_f8f6f4 v[120:123], v[138:145], v[160:167], v[36:39], v154, v154 op_sel_hi:[0,0,0]
	v_mfma_scale_f32_16x16x128_f8f6f4 v[124:127], v[124:131], v[168:175], v[72:75], v154, v154 op_sel_hi:[0,0,0]
	v_mfma_scale_f32_16x16x128_f8f6f4 v[128:131], v[138:145], v[168:175], v[76:79], v154, v154 op_sel_hi:[0,0,0]
	s_setprio 0
	s_barrier
	s_add_u32 s2, s20, 0x300
	s_addc_u32 s3, s21, 0
	ds_read_b128 v[138:141], v132
	ds_read_b128 v[142:145], v132 offset:1024
	ds_read_b128 v[160:163], v132 offset:2048
	ds_read_b128 v[164:167], v132 offset:3072
	ds_read_b128 v[168:171], v158
	ds_read_b128 v[172:175], v158 offset:1024
	ds_read_b128 v[176:179], v158 offset:2048
	ds_read_b128 v[180:183], v158 offset:3072
	ds_read_b128 v[184:187], v158 offset:4096
	ds_read_b128 v[188:191], v158 offset:5120
	ds_read_b128 v[192:195], v158 offset:6144
	ds_read_b128 v[196:199], v158 offset:7168
	s_add_u32 s94, s8, 0x280
	s_addc_u32 s95, s9, 0
	v_and_b32_e32 v34, 0xffff, v255
	v_lshl_add_u32 v34, v34, 10, v155
	s_mov_b32 m0, s23
	s_nop 0
	global_load_lds_dwordx4 v34, s[94:95]
	v_lshrrev_b32_e32 v34, 16, v255
	v_lshl_add_u32 v34, v34, 10, v155
	s_mov_b32 m0, s17
	s_nop 0
	global_load_lds_dwordx4 v34, s[94:95]
	s_waitcnt lgkmcnt(8)
	s_barrier
	s_waitcnt lgkmcnt(0)
	s_setprio 1
	s_waitcnt lgkmcnt(0)
	v_mfma_scale_f32_16x16x128_f8f6f4 v[204:207], v[138:145], v[192:199], v[204:207], v154, v154 op_sel_hi:[0,0,0]
	v_mfma_scale_f32_16x16x128_f8f6f4 v[146:149], v[138:145], v[168:175], v[2:5], v154, v154 op_sel_hi:[0,0,0]
	v_mfma_scale_f32_16x16x128_f8f6f4 v[224:227], v[160:167], v[168:175], v[6:9], v154, v154 op_sel_hi:[0,0,0]
	v_mfma_scale_f32_16x16x128_f8f6f4 v[228:231], v[138:145], v[176:183], v[10:13], v154, v154 op_sel_hi:[0,0,0]
	v_mfma_scale_f32_16x16x128_f8f6f4 v[232:235], v[160:167], v[176:183], v[14:17], v154, v154 op_sel_hi:[0,0,0]
	v_mfma_scale_f32_16x16x128_f8f6f4 v[150:153], v[138:145], v[184:191], v[150:153], v154, v154 op_sel_hi:[0,0,0]
	v_mfma_scale_f32_16x16x128_f8f6f4 v[200:203], v[160:167], v[184:191], v[200:203], v154, v154 op_sel_hi:[0,0,0]
	v_mfma_scale_f32_16x16x128_f8f6f4 v[208:211], v[160:167], v[192:199], v[208:211], v154, v154 op_sel_hi:[0,0,0]
	s_setprio 0
	s_barrier
	s_add_u32 s74, s20, 0x10300
	s_addc_u32 s75, s21, 0
	s_mov_b32 m0, s44
	ds_read_b128 v[2:5], v133
	ds_read_b128 v[6:9], v133 offset:1024
	ds_read_b128 v[10:13], v133 offset:2048
	ds_read_b128 v[14:17], v133 offset:3072
	s_nop 0
	v_lshl_add_u64 v[18:19], s[2:3], 0, v[252:253]
	global_load_lds_dwordx4 v[18:19], off
	v_lshl_add_u64 v[18:19], s[74:75], 0, v[252:253]
	s_mov_b32 m0, s45
	s_nop 0
	global_load_lds_dwordx4 v[18:19], off
	s_barrier
	s_waitcnt lgkmcnt(0)
	s_setprio 1
	s_waitcnt lgkmcnt(0)
	v_mfma_scale_f32_16x16x128_f8f6f4 v[64:67], v[10:17], v[192:199], v[64:67], v154, v154 op_sel_hi:[0,0,0]
	v_mfma_scale_f32_16x16x128_f8f6f4 v[212:215], v[2:9], v[168:175], v[212:215], v154, v154 op_sel_hi:[0,0,0]
	v_mfma_scale_f32_16x16x128_f8f6f4 v[168:171], v[10:17], v[168:175], v[40:43], v154, v154 op_sel_hi:[0,0,0]
	v_mfma_scale_f32_16x16x128_f8f6f4 v[172:175], v[2:9], v[176:183], v[44:47], v154, v154 op_sel_hi:[0,0,0]
	v_mfma_scale_f32_16x16x128_f8f6f4 v[176:179], v[10:17], v[176:183], v[48:51], v154, v154 op_sel_hi:[0,0,0]
	v_mfma_scale_f32_16x16x128_f8f6f4 v[180:183], v[2:9], v[184:191], v[52:55], v154, v154 op_sel_hi:[0,0,0]
	v_mfma_scale_f32_16x16x128_f8f6f4 v[184:187], v[10:17], v[184:191], v[56:59], v154, v154 op_sel_hi:[0,0,0]
	v_mfma_scale_f32_16x16x128_f8f6f4 v[188:191], v[2:9], v[192:199], v[60:63], v154, v154 op_sel_hi:[0,0,0]
	s_setprio 0
	s_barrier
	s_nop 2
	s_mov_b64 s[76:77], 0x300
	ds_read_b128 v[18:21], v158 offset:16384
	ds_read_b128 v[22:25], v158 offset:17408
	ds_read_b128 v[26:29], v158 offset:18432
	ds_read_b128 v[30:33], v158 offset:19456
	ds_read_b128 v[36:39], v158 offset:20480
	ds_read_b128 v[40:43], v158 offset:21504
	ds_read_b128 v[44:47], v158 offset:22528
	ds_read_b128 v[48:51], v158 offset:23552
	s_add_u32 s94, s8, 0x300
	s_addc_u32 s95, s9, 0
	v_and_b32_e32 v34, 0xffff, v159
	v_lshl_add_u32 v34, v34, 10, v155
	s_mov_b32 m0, s47
	s_nop 0
	global_load_lds_dwordx4 v34, s[94:95]
	v_lshrrev_b32_e32 v34, 16, v159
	v_lshl_add_u32 v34, v34, 10, v155
	s_mov_b32 m0, s48
	s_nop 0
	global_load_lds_dwordx4 v34, s[94:95]
	s_barrier
	s_waitcnt lgkmcnt(0)
	s_setprio 1
	s_waitcnt lgkmcnt(0)
	v_mfma_scale_f32_16x16x128_f8f6f4 v[236:239], v[138:145], v[36:43], v[84:87], v154, v154 op_sel_hi:[0,0,0]
	v_mfma_scale_f32_16x16x128_f8f6f4 v[240:243], v[160:167], v[36:43], v[88:91], v154, v154 op_sel_hi:[0,0,0]
	v_mfma_scale_f32_16x16x128_f8f6f4 v[192:195], v[138:145], v[18:25], v[68:71], v154, v154 op_sel_hi:[0,0,0]
	v_mfma_scale_f32_16x16x128_f8f6f4 v[196:199], v[160:167], v[18:25], v[216:219], v154, v154 op_sel_hi:[0,0,0]
	v_mfma_scale_f32_16x16x128_f8f6f4 v[216:219], v[138:145], v[26:33], v[220:223], v154, v154 op_sel_hi:[0,0,0]
	v_mfma_scale_f32_16x16x128_f8f6f4 v[220:223], v[160:167], v[26:33], v[80:83], v154, v154 op_sel_hi:[0,0,0]
	v_mfma_scale_f32_16x16x128_f8f6f4 v[138:141], v[138:145], v[44:51], v[92:95], v154, v154 op_sel_hi:[0,0,0]
	v_mfma_scale_f32_16x16x128_f8f6f4 v[142:145], v[160:167], v[44:51], v[96:99], v154, v154 op_sel_hi:[0,0,0]
	s_setprio 0
	s_barrier
	s_add_u32 s2, s20, 0x20300
	s_addc_u32 s3, s21, 0
	s_add_u32 s74, s20, 0x30300
	s_addc_u32 s75, s21, 0
	s_mov_b32 m0, s50
	s_nop 0
	v_lshl_add_u64 v[52:53], s[2:3], 0, v[252:253]
	global_load_lds_dwordx4 v[52:53], off
	v_lshl_add_u64 v[52:53], s[74:75], 0, v[252:253]
	s_mov_b32 m0, s51
	s_nop 0
	global_load_lds_dwordx4 v[52:53], off
	s_waitcnt vmcnt(6)
	s_barrier
	s_setprio 1
	v_mfma_scale_f32_16x16x128_f8f6f4 v[160:163], v[2:9], v[18:25], v[100:103], v154, v154 op_sel_hi:[0,0,0]
	v_mfma_scale_f32_16x16x128_f8f6f4 v[164:167], v[10:17], v[18:25], v[104:107], v154, v154 op_sel_hi:[0,0,0]
	v_mfma_scale_f32_16x16x128_f8f6f4 v[244:247], v[2:9], v[26:33], v[108:111], v154, v154 op_sel_hi:[0,0,0]
	v_mfma_scale_f32_16x16x128_f8f6f4 v[248:251], v[10:17], v[26:33], v[112:115], v154, v154 op_sel_hi:[0,0,0]
	v_mfma_scale_f32_16x16x128_f8f6f4 v[18:21], v[2:9], v[36:43], v[116:119], v154, v154 op_sel_hi:[0,0,0]
	v_mfma_scale_f32_16x16x128_f8f6f4 v[22:25], v[10:17], v[36:43], v[120:123], v154, v154 op_sel_hi:[0,0,0]
	v_mfma_scale_f32_16x16x128_f8f6f4 v[6:9], v[2:9], v[44:51], v[124:127], v154, v154 op_sel_hi:[0,0,0]
	v_mfma_scale_f32_16x16x128_f8f6f4 v[10:13], v[10:17], v[44:51], v[128:131], v154, v154 op_sel_hi:[0,0,0]
	s_setprio 0
	s_barrier
	ds_read_b128 v[68:71], v135
	ds_read_b128 v[72:75], v135 offset:1024
	ds_read_b128 v[76:79], v135 offset:2048
	ds_read_b128 v[80:83], v135 offset:3072
	ds_read_b128 v[40:43], v158 offset:32768
	ds_read_b128 v[44:47], v158 offset:33792
	ds_read_b128 v[48:51], v158 offset:34816
	ds_read_b128 v[52:55], v158 offset:35840
	ds_read_b128 v[56:59], v158 offset:36864
	ds_read_b128 v[60:63], v158 offset:37888
	ds_read_b128 v[84:87], v158 offset:38912
	ds_read_b128 v[88:91], v158 offset:39936
	s_add_u32 s94, s8, 0x300
	s_addc_u32 s95, s9, 0
	v_and_b32_e32 v34, 0xffff, v255
	v_lshl_add_u32 v34, v34, 10, v155
	s_mov_b32 m0, s52
	s_nop 0
	global_load_lds_dwordx4 v34, s[94:95]
	v_lshrrev_b32_e32 v34, 16, v255
	v_lshl_add_u32 v34, v34, 10, v155
	s_mov_b32 m0, s53
	s_nop 0
	global_load_lds_dwordx4 v34, s[94:95]
	s_waitcnt lgkmcnt(8)
	s_barrier
	s_waitcnt lgkmcnt(0)
	s_setprio 1
	s_waitcnt lgkmcnt(0)
	v_mfma_scale_f32_16x16x128_f8f6f4 v[2:5], v[68:75], v[40:47], v[146:149], v154, v154 op_sel_hi:[0,0,0]
	v_mfma_scale_f32_16x16x128_f8f6f4 v[14:17], v[76:83], v[48:55], v[232:235], v154, v154 op_sel_hi:[0,0,0]
	v_mfma_scale_f32_16x16x128_f8f6f4 v[26:29], v[68:75], v[84:91], v[204:207], v154, v154 op_sel_hi:[0,0,0]
	v_mfma_scale_f32_16x16x128_f8f6f4 v[30:33], v[76:83], v[84:91], v[208:211], v154, v154 op_sel_hi:[0,0,0]
	v_mfma_scale_f32_16x16x128_f8f6f4 v[224:227], v[76:83], v[40:47], v[224:227], v154, v154 op_sel_hi:[0,0,0]
	v_mfma_scale_f32_16x16x128_f8f6f4 v[228:231], v[68:75], v[48:55], v[228:231], v154, v154 op_sel_hi:[0,0,0]
	v_mfma_scale_f32_16x16x128_f8f6f4 v[146:149], v[68:75], v[56:63], v[150:153], v154, v154 op_sel_hi:[0,0,0]
	v_mfma_scale_f32_16x16x128_f8f6f4 v[150:153], v[76:83], v[56:63], v[200:203], v154, v154 op_sel_hi:[0,0,0]
	s_setprio 0
	s_barrier
; template <class Epi, class Src>
; __device__ __forceinline__ void gemm_phase(LAS unsigned char* lds, const Src S, const Epi E) {
;     ...
;         for (int t = 0; t < NKTR - 2; t += 2) {
;             const size_t k1 = (size_t)(t + 1) * kstep, k2 = (size_t)(t + 2) * kstep;
;             const char* b2 = cB + k2; const char* b3 = b2 + kstep;
;             G8_ITER(cA, par, k1, cA, par, k2, b2, b3);
;         }
;         {
;             const int par2 = has_next ? (par ^ 1) : par;
;             const char* b3 = nB + kstep;
;             G8_ITER(cA, par, (size_t)(NKTR - 1) * kstep, nA, par2, (size_t)0, nB, b3);
;         }
	s_add_u32 s2, s20, 0x380
	s_addc_u32 s3, s21, 0
	s_add_u32 s74, s20, 0x10380
	s_addc_u32 s75, s21, 0
	s_mov_b32 m0, s59
	ds_read_b128 v[92:95], v136
	ds_read_b128 v[96:99], v136 offset:1024
	ds_read_b128 v[100:103], v136 offset:2048
	ds_read_b128 v[104:107], v136 offset:3072
	s_nop 0
	v_lshl_add_u64 v[36:37], s[2:3], 0, v[252:253]
	global_load_lds_dwordx4 v[36:37], off
	v_lshl_add_u64 v[36:37], s[74:75], 0, v[252:253]
	s_mov_b32 m0, s60
	s_nop 0
	global_load_lds_dwordx4 v[36:37], off
	s_barrier
	s_waitcnt lgkmcnt(0)
	s_setprio 1
	s_waitcnt lgkmcnt(0)
	v_mfma_scale_f32_16x16x128_f8f6f4 v[36:39], v[92:99], v[40:47], v[212:215], v154, v154 op_sel_hi:[0,0,0]
	v_mfma_scale_f32_16x16x128_f8f6f4 v[40:43], v[100:107], v[40:47], v[168:171], v154, v154 op_sel_hi:[0,0,0]
	v_mfma_scale_f32_16x16x128_f8f6f4 v[44:47], v[92:99], v[48:55], v[172:175], v154, v154 op_sel_hi:[0,0,0]
	v_mfma_scale_f32_16x16x128_f8f6f4 v[48:51], v[100:107], v[48:55], v[176:179], v154, v154 op_sel_hi:[0,0,0]
	v_mfma_scale_f32_16x16x128_f8f6f4 v[52:55], v[92:99], v[56:63], v[180:183], v154, v154 op_sel_hi:[0,0,0]
	v_mfma_scale_f32_16x16x128_f8f6f4 v[56:59], v[100:107], v[56:63], v[184:187], v154, v154 op_sel_hi:[0,0,0]
	v_mfma_scale_f32_16x16x128_f8f6f4 v[60:63], v[92:99], v[84:91], v[188:191], v154, v154 op_sel_hi:[0,0,0]
	v_mfma_scale_f32_16x16x128_f8f6f4 v[64:67], v[100:107], v[84:91], v[64:67], v154, v154 op_sel_hi:[0,0,0]
	s_setprio 0
	s_barrier
	s_mov_b64 s[76:77], 0x380
	ds_read_b128 v[84:87], v158 offset:49152
	ds_read_b128 v[88:91], v158 offset:50176
	ds_read_b128 v[108:111], v158 offset:51200
	ds_read_b128 v[112:115], v158 offset:52224
	ds_read_b128 v[116:119], v158 offset:53248
	ds_read_b128 v[120:123], v158 offset:54272
	ds_read_b128 v[124:127], v158 offset:55296
	ds_read_b128 v[128:131], v158 offset:56320
	s_add_u32 s94, s8, 0x380
	s_addc_u32 s95, s9, 0
	v_and_b32_e32 v34, 0xffff, v159
	v_lshl_add_u32 v34, v34, 10, v155
	s_mov_b32 m0, s61
	s_nop 0
	global_load_lds_dwordx4 v34, s[94:95]
	v_lshrrev_b32_e32 v34, 16, v159
	v_lshl_add_u32 v34, v34, 10, v155
	s_mov_b32 m0, s62
	s_nop 0
	global_load_lds_dwordx4 v34, s[94:95]
	s_barrier
	s_waitcnt lgkmcnt(0)
	s_setprio 1
	s_waitcnt lgkmcnt(0)
	v_mfma_scale_f32_16x16x128_f8f6f4 v[168:171], v[68:75], v[84:91], v[192:195], v154, v154 op_sel_hi:[0,0,0]
	v_mfma_scale_f32_16x16x128_f8f6f4 v[172:175], v[76:83], v[84:91], v[196:199], v154, v154 op_sel_hi:[0,0,0]
	v_mfma_scale_f32_16x16x128_f8f6f4 v[176:179], v[68:75], v[108:115], v[216:219], v154, v154 op_sel_hi:[0,0,0]
	v_mfma_scale_f32_16x16x128_f8f6f4 v[180:183], v[76:83], v[108:115], v[220:223], v154, v154 op_sel_hi:[0,0,0]
	v_mfma_scale_f32_16x16x128_f8f6f4 v[184:187], v[68:75], v[116:123], v[236:239], v154, v154 op_sel_hi:[0,0,0]
	v_mfma_scale_f32_16x16x128_f8f6f4 v[188:191], v[76:83], v[116:123], v[240:243], v154, v154 op_sel_hi:[0,0,0]
	v_mfma_scale_f32_16x16x128_f8f6f4 v[138:141], v[68:75], v[124:131], v[138:141], v154, v154 op_sel_hi:[0,0,0]
	v_mfma_scale_f32_16x16x128_f8f6f4 v[142:145], v[76:83], v[124:131], v[142:145], v154, v154 op_sel_hi:[0,0,0]
	s_setprio 0
	s_barrier
	s_add_u32 s2, s20, 0x20380
	s_addc_u32 s3, s21, 0
	s_add_u32 s74, s20, 0x30380
	s_addc_u32 s75, s21, 0
	s_mov_b32 m0, s64
	s_nop 0
	v_lshl_add_u64 v[68:69], s[2:3], 0, v[252:253]
	global_load_lds_dwordx4 v[68:69], off
	v_lshl_add_u64 v[68:69], s[74:75], 0, v[252:253]
	s_mov_b32 m0, s65
	s_nop 0
	global_load_lds_dwordx4 v[68:69], off
	s_waitcnt vmcnt(6)
	s_barrier
	s_setprio 1
	v_mfma_scale_f32_16x16x128_f8f6f4 v[200:203], v[92:99], v[116:123], v[18:21], v154, v154 op_sel_hi:[0,0,0]
	v_mfma_scale_f32_16x16x128_f8f6f4 v[116:119], v[100:107], v[116:123], v[22:25], v154, v154 op_sel_hi:[0,0,0]
	v_mfma_scale_f32_16x16x128_f8f6f4 v[120:123], v[92:99], v[124:131], v[6:9], v154, v154 op_sel_hi:[0,0,0]
	v_mfma_scale_f32_16x16x128_f8f6f4 v[124:127], v[100:107], v[124:131], v[10:13], v154, v154 op_sel_hi:[0,0,0]
	v_mfma_scale_f32_16x16x128_f8f6f4 v[160:163], v[92:99], v[84:91], v[160:163], v154, v154 op_sel_hi:[0,0,0]
	v_mfma_scale_f32_16x16x128_f8f6f4 v[164:167], v[100:107], v[84:91], v[164:167], v154, v154 op_sel_hi:[0,0,0]
	v_mfma_scale_f32_16x16x128_f8f6f4 v[192:195], v[92:99], v[108:115], v[244:247], v154, v154 op_sel_hi:[0,0,0]
	v_mfma_scale_f32_16x16x128_f8f6f4 v[196:199], v[100:107], v[108:115], v[248:251], v154, v154 op_sel_hi:[0,0,0]
	s_setprio 0
	s_barrier
	s_xor_b32 s3, s68, 1
	s_and_b64 s[74:75], s[24:25], exec
	s_cselect_b32 s2, s3, s68
	ds_read_b128 v[68:71], v132
	ds_read_b128 v[72:75], v132 offset:1024
	ds_read_b128 v[76:79], v132 offset:2048
	ds_read_b128 v[80:83], v132 offset:3072
	ds_read_b128 v[84:87], v158
	ds_read_b128 v[88:91], v158 offset:1024
	ds_read_b128 v[92:95], v158 offset:2048
	ds_read_b128 v[96:99], v158 offset:3072
	ds_read_b128 v[100:103], v158 offset:4096
	ds_read_b128 v[104:107], v158 offset:5120
	ds_read_b128 v[108:111], v158 offset:6144
	ds_read_b128 v[112:115], v158 offset:7168
	s_add_u32 s94, s8, 0x380
	s_addc_u32 s95, s9, 0
	v_and_b32_e32 v34, 0xffff, v255
	v_lshl_add_u32 v34, v34, 10, v155
	s_mov_b32 m0, s23
	s_nop 0
	global_load_lds_dwordx4 v34, s[94:95]
	v_lshrrev_b32_e32 v34, 16, v255
	v_lshl_add_u32 v34, v34, 10, v155
	s_mov_b32 m0, s17
	s_nop 0
	global_load_lds_dwordx4 v34, s[94:95]
	s_waitcnt lgkmcnt(8)
	s_barrier
; template <class Epi, class Src>
; __device__ __forceinline__ void gemm_phase(LAS unsigned char* lds, const Src S, const Epi E) {
;     ...
;         {
;             const int par2 = has_next ? (par ^ 1) : par;
;             const char* b3 = nB + kstep;
;             G8_ITER(cA, par, (size_t)(NKTR - 1) * kstep, nA, par2, (size_t)0, nB, b3);
;         }
	s_waitcnt lgkmcnt(0)
	s_setprio 1
	s_waitcnt lgkmcnt(0)
	v_mfma_scale_f32_16x16x128_f8f6f4 v[128:131], v[68:75], v[84:91], v[2:5], v154, v154 op_sel_hi:[0,0,0]
	v_mfma_scale_f32_16x16x128_f8f6f4 v[204:207], v[76:83], v[84:91], v[224:227], v154, v154 op_sel_hi:[0,0,0]
	v_mfma_scale_f32_16x16x128_f8f6f4 v[208:211], v[68:75], v[92:99], v[228:231], v154, v154 op_sel_hi:[0,0,0]
	v_mfma_scale_f32_16x16x128_f8f6f4 v[212:215], v[76:83], v[92:99], v[14:17], v154, v154 op_sel_hi:[0,0,0]
	v_mfma_scale_f32_16x16x128_f8f6f4 v[146:149], v[68:75], v[100:107], v[146:149], v154, v154 op_sel_hi:[0,0,0]
	v_mfma_scale_f32_16x16x128_f8f6f4 v[150:153], v[76:83], v[100:107], v[150:153], v154, v154 op_sel_hi:[0,0,0]
	v_mfma_scale_f32_16x16x128_f8f6f4 v[216:219], v[68:75], v[108:115], v[26:29], v154, v154 op_sel_hi:[0,0,0]
	v_mfma_scale_f32_16x16x128_f8f6f4 v[220:223], v[76:83], v[108:115], v[30:33], v154, v154 op_sel_hi:[0,0,0]
	s_setprio 0
	s_barrier
	s_add_u32 s74, s0, 0x10000
	s_addc_u32 s75, s1, 0
	s_mov_b64 s[76:77], s[0:1]
	s_mov_b32 m0, s44
	ds_read_b128 v[2:5], v133
	ds_read_b128 v[6:9], v133 offset:1024
	ds_read_b128 v[10:13], v133 offset:2048
	ds_read_b128 v[14:17], v133 offset:3072
	s_nop 0
	v_lshl_add_u64 v[18:19], s[76:77], 0, v[252:253]
	global_load_lds_dwordx4 v[18:19], off
	v_lshl_add_u64 v[18:19], s[74:75], 0, v[252:253]
	s_mov_b32 m0, s45
	s_nop 0
	global_load_lds_dwordx4 v[18:19], off
	s_barrier
	s_waitcnt lgkmcnt(0)
	s_setprio 1
	s_waitcnt lgkmcnt(0)
	v_mfma_scale_f32_16x16x128_f8f6f4 v[224:227], v[2:9], v[84:91], v[36:39], v154, v154 op_sel_hi:[0,0,0]
	v_mfma_scale_f32_16x16x128_f8f6f4 v[84:87], v[10:17], v[84:91], v[40:43], v154, v154 op_sel_hi:[0,0,0]
	v_mfma_scale_f32_16x16x128_f8f6f4 v[88:91], v[2:9], v[92:99], v[44:47], v154, v154 op_sel_hi:[0,0,0]
	v_mfma_scale_f32_16x16x128_f8f6f4 v[52:55], v[2:9], v[100:107], v[52:55], v154, v154 op_sel_hi:[0,0,0]
	v_mfma_scale_f32_16x16x128_f8f6f4 v[56:59], v[10:17], v[100:107], v[56:59], v154, v154 op_sel_hi:[0,0,0]
	v_mfma_scale_f32_16x16x128_f8f6f4 v[60:63], v[2:9], v[108:115], v[60:63], v154, v154 op_sel_hi:[0,0,0]
	v_mfma_scale_f32_16x16x128_f8f6f4 v[64:67], v[10:17], v[108:115], v[64:67], v154, v154 op_sel_hi:[0,0,0]
	v_mfma_scale_f32_16x16x128_f8f6f4 v[228:231], v[10:17], v[92:99], v[48:51], v154, v154 op_sel_hi:[0,0,0]
	s_setprio 0
	v_lshl_add_u32 v34, s2, 10, v156
	s_barrier
	ds_read2st64_b32 v[92:93], v34 offset1:1
	ds_read_b128 v[18:21], v158 offset:16384
	ds_read_b128 v[22:25], v158 offset:17408
	ds_read_b128 v[26:29], v158 offset:18432
	ds_read_b128 v[30:33], v158 offset:19456
	ds_read_b128 v[36:39], v158 offset:20480
	ds_read_b128 v[40:43], v158 offset:21504
	ds_read_b128 v[44:47], v158 offset:22528
	ds_read_b128 v[48:51], v158 offset:23552
	s_mov_b32 m0, s47
	s_waitcnt lgkmcnt(8)
	v_lshl_or_b32 v159, v93, 16, v92
	v_lshl_add_u32 v92, v92, 10, v155
	global_load_lds_dwordx4 v92, s[8:9]
	v_lshl_add_u32 v92, v93, 10, v155
	s_mov_b32 m0, s48
	s_nop 0
	global_load_lds_dwordx4 v92, s[8:9]
	s_barrier
	s_waitcnt lgkmcnt(0)
	s_setprio 1
	s_waitcnt lgkmcnt(0)
	v_mfma_scale_f32_16x16x128_f8f6f4 v[236:239], v[76:83], v[18:25], v[172:175], v154, v154 op_sel_hi:[0,0,0]
	v_mfma_scale_f32_16x16x128_f8f6f4 v[240:243], v[68:75], v[26:33], v[176:179], v154, v154 op_sel_hi:[0,0,0]
	v_mfma_scale_f32_16x16x128_f8f6f4 v[244:247], v[76:83], v[26:33], v[180:183], v154, v154 op_sel_hi:[0,0,0]
	v_mfma_scale_f32_16x16x128_f8f6f4 v[248:251], v[68:75], v[36:43], v[184:187], v154, v154 op_sel_hi:[0,0,0]
	v_mfma_scale_f32_16x16x128_f8f6f4 v[92:95], v[76:83], v[36:43], v[188:191], v154, v154 op_sel_hi:[0,0,0]
	v_mfma_scale_f32_16x16x128_f8f6f4 v[232:235], v[68:75], v[18:25], v[168:171], v154, v154 op_sel_hi:[0,0,0]
	v_mfma_scale_f32_16x16x128_f8f6f4 v[72:75], v[68:75], v[44:51], v[138:141], v154, v154 op_sel_hi:[0,0,0]
	v_mfma_scale_f32_16x16x128_f8f6f4 v[76:79], v[76:83], v[44:51], v[142:145], v154, v154 op_sel_hi:[0,0,0]
	s_setprio 0
	s_barrier
	s_add_u32 s74, s0, 0x20000
	s_addc_u32 s75, s1, 0
	s_add_u32 s76, s0, 0x30000
	s_addc_u32 s77, s1, 0
	s_mov_b32 m0, s50
	s_nop 0
	v_lshl_add_u64 v[68:69], s[74:75], 0, v[252:253]
	global_load_lds_dwordx4 v[68:69], off
	v_lshl_add_u64 v[68:69], s[76:77], 0, v[252:253]
	s_mov_b32 m0, s51
	s_nop 0
	global_load_lds_dwordx4 v[68:69], off
	s_waitcnt vmcnt(6)
	s_barrier
	s_setprio 1
	v_mfma_scale_f32_16x16x128_f8f6f4 v[80:83], v[2:9], v[18:25], v[160:163], v154, v154 op_sel_hi:[0,0,0]
	v_mfma_scale_f32_16x16x128_f8f6f4 v[96:99], v[10:17], v[36:43], v[116:119], v154, v154 op_sel_hi:[0,0,0]
	v_mfma_scale_f32_16x16x128_f8f6f4 v[68:71], v[10:17], v[18:25], v[164:167], v154, v154 op_sel_hi:[0,0,0]
	v_mfma_scale_f32_16x16x128_f8f6f4 v[192:195], v[2:9], v[26:33], v[192:195], v154, v154 op_sel_hi:[0,0,0]
	v_mfma_scale_f32_16x16x128_f8f6f4 v[196:199], v[10:17], v[26:33], v[196:199], v154, v154 op_sel_hi:[0,0,0]
	v_mfma_scale_f32_16x16x128_f8f6f4 v[200:203], v[2:9], v[36:43], v[200:203], v154, v154 op_sel_hi:[0,0,0]
	v_mfma_scale_f32_16x16x128_f8f6f4 v[100:103], v[2:9], v[44:51], v[120:123], v154, v154 op_sel_hi:[0,0,0]
	v_mfma_scale_f32_16x16x128_f8f6f4 v[104:107], v[10:17], v[44:51], v[124:127], v154, v154 op_sel_hi:[0,0,0]
	s_setprio 0
	s_barrier
	ds_read2st64_b32 v[108:109], v34 offset0:2 offset1:3
	ds_read_b128 v[2:5], v135
	ds_read_b128 v[6:9], v135 offset:1024
	ds_read_b128 v[10:13], v135 offset:2048
	ds_read_b128 v[14:17], v135 offset:3072
	ds_read_b128 v[18:21], v158 offset:32768
	ds_read_b128 v[22:25], v158 offset:33792
	ds_read_b128 v[26:29], v158 offset:34816
	ds_read_b128 v[30:33], v158 offset:35840
	ds_read_b128 v[36:39], v158 offset:36864
	ds_read_b128 v[40:43], v158 offset:37888
	ds_read_b128 v[44:47], v158 offset:38912
	ds_read_b128 v[48:51], v158 offset:39936
	s_mov_b32 m0, s52
	s_waitcnt lgkmcnt(12)
	v_lshl_or_b32 v255, v109, 16, v108
	v_lshl_add_u32 v108, v108, 10, v155
	global_load_lds_dwordx4 v108, s[8:9]
	v_lshl_add_u32 v108, v109, 10, v155
	s_mov_b32 m0, s53
	s_nop 0
	global_load_lds_dwordx4 v108, s[8:9]
	s_waitcnt lgkmcnt(8)
	s_barrier
; #define lds lds_hidden(lds0)
; template <class Epi, class Src>
; __device__ __forceinline__ void gemm_phase(LAS unsigned char* lds, const Src S, const Epi E) {
;     ...
;             G8_ITER(cA, par, (size_t)(NKTR - 1) * kstep, nA, par2, (size_t)0, nB, b3);
;         }
;     ...
;         { int tz = threadIdx.x; asm volatile("" : "+v"(tz));
;           const int wid2 = __builtin_amdgcn_readfirstlane(tz >> 6), lane2 = tz & 63;
;           E(acc, cur, wid2 >> 2, wid2 & 3, lane2 & 15, lane2 >> 4, lds, par); }
	s_waitcnt lgkmcnt(0)
	s_setprio 1
	s_waitcnt lgkmcnt(0)
	v_mfma_scale_f32_16x16x128_f8f6f4 v[128:131], v[2:9], v[18:25], v[128:131], v154, v154 op_sel_hi:[0,0,0]
	v_mfma_scale_f32_16x16x128_f8f6f4 v[124:127], v[10:17], v[18:25], v[204:207], v154, v154 op_sel_hi:[0,0,0]
	v_mfma_scale_f32_16x16x128_f8f6f4 v[120:123], v[2:9], v[26:33], v[208:211], v154, v154 op_sel_hi:[0,0,0]
	v_mfma_scale_f32_16x16x128_f8f6f4 v[116:119], v[10:17], v[26:33], v[212:215], v154, v154 op_sel_hi:[0,0,0]
	v_mfma_scale_f32_16x16x128_f8f6f4 v[112:115], v[2:9], v[36:43], v[146:149], v154, v154 op_sel_hi:[0,0,0]
	v_mfma_scale_f32_16x16x128_f8f6f4 v[108:111], v[10:17], v[36:43], v[150:153], v154, v154 op_sel_hi:[0,0,0]
	v_mfma_scale_f32_16x16x128_f8f6f4 v[204:207], v[2:9], v[44:51], v[216:219], v154, v154 op_sel_hi:[0,0,0]
	v_mfma_scale_f32_16x16x128_f8f6f4 v[208:211], v[10:17], v[44:51], v[220:223], v154, v154 op_sel_hi:[0,0,0]
	s_setprio 0
	s_barrier
	s_add_u32 s74, s0, 0x80
	s_addc_u32 s75, s1, 0
	s_add_u32 s76, s0, 0x10080
	s_addc_u32 s77, s1, 0
	s_mov_b32 m0, s59
	ds_read_b128 v[138:141], v136
	ds_read_b128 v[142:145], v136 offset:1024
	ds_read_b128 v[160:163], v136 offset:2048
	ds_read_b128 v[164:167], v136 offset:3072
	s_nop 0
	v_lshl_add_u64 v[132:133], s[74:75], 0, v[252:253]
	global_load_lds_dwordx4 v[132:133], off
	v_lshl_add_u64 v[132:133], s[76:77], 0, v[252:253]
	s_mov_b32 m0, s60
	s_nop 0
	global_load_lds_dwordx4 v[132:133], off
	s_barrier
	s_waitcnt lgkmcnt(0)
	s_setprio 1
	s_waitcnt lgkmcnt(0)
	v_mfma_scale_f32_16x16x128_f8f6f4 v[84:87], v[160:167], v[18:25], v[84:87], v154, v154 op_sel_hi:[0,0,0]
	v_mfma_scale_f32_16x16x128_f8f6f4 v[88:91], v[138:145], v[26:33], v[88:91], v154, v154 op_sel_hi:[0,0,0]
	v_mfma_scale_f32_16x16x128_f8f6f4 v[26:29], v[160:167], v[26:33], v[228:231], v154, v154 op_sel_hi:[0,0,0]
	v_mfma_scale_f32_16x16x128_f8f6f4 v[52:55], v[138:145], v[36:43], v[52:55], v154, v154 op_sel_hi:[0,0,0]
	v_mfma_scale_f32_16x16x128_f8f6f4 v[36:39], v[160:167], v[36:43], v[56:59], v154, v154 op_sel_hi:[0,0,0]
	v_mfma_scale_f32_16x16x128_f8f6f4 v[30:33], v[138:145], v[44:51], v[60:63], v154, v154 op_sel_hi:[0,0,0]
	v_mfma_scale_f32_16x16x128_f8f6f4 v[40:43], v[160:167], v[44:51], v[64:67], v154, v154 op_sel_hi:[0,0,0]
	v_mfma_scale_f32_16x16x128_f8f6f4 v[132:135], v[138:145], v[18:25], v[224:227], v154, v154 op_sel_hi:[0,0,0]
	s_setprio 0
	s_barrier
	ds_read_b128 v[18:21], v158 offset:49152
	ds_read_b128 v[22:25], v158 offset:50176
	ds_read_b128 v[168:171], v158 offset:51200
	ds_read_b128 v[172:175], v158 offset:52224
	ds_read_b128 v[176:179], v158 offset:53248
	ds_read_b128 v[180:183], v158 offset:54272
	ds_read_b128 v[184:187], v158 offset:55296
	ds_read_b128 v[188:191], v158 offset:56320
	s_add_u32 s94, s8, 0x80
	s_addc_u32 s95, s9, 0
	v_and_b32_e32 v34, 0xffff, v159
	v_lshl_add_u32 v34, v34, 10, v155
	s_mov_b32 m0, s61
	s_nop 0
	global_load_lds_dwordx4 v34, s[94:95]
	v_lshrrev_b32_e32 v34, 16, v159
	v_lshl_add_u32 v34, v34, 10, v155
	s_mov_b32 m0, s62
	s_nop 0
	global_load_lds_dwordx4 v34, s[94:95]
	s_barrier
	s_waitcnt lgkmcnt(0)
	s_setprio 1
	s_waitcnt lgkmcnt(0)
	v_mfma_scale_f32_16x16x128_f8f6f4 v[64:67], v[2:9], v[18:25], v[232:235], v154, v154 op_sel_hi:[0,0,0]
	v_mfma_scale_f32_16x16x128_f8f6f4 v[60:63], v[10:17], v[18:25], v[236:239], v154, v154 op_sel_hi:[0,0,0]
	v_mfma_scale_f32_16x16x128_f8f6f4 v[56:59], v[2:9], v[168:175], v[240:243], v154, v154 op_sel_hi:[0,0,0]
	v_mfma_scale_f32_16x16x128_f8f6f4 v[236:239], v[10:17], v[168:175], v[244:247], v154, v154 op_sel_hi:[0,0,0]
	v_mfma_scale_f32_16x16x128_f8f6f4 v[48:51], v[2:9], v[176:183], v[248:251], v154, v154 op_sel_hi:[0,0,0]
	v_mfma_scale_f32_16x16x128_f8f6f4 v[44:47], v[10:17], v[176:183], v[92:95], v154, v154 op_sel_hi:[0,0,0]
	v_mfma_scale_f32_16x16x128_f8f6f4 v[6:9], v[2:9], v[184:191], v[72:75], v154, v154 op_sel_hi:[0,0,0]
	v_mfma_scale_f32_16x16x128_f8f6f4 v[244:247], v[10:17], v[184:191], v[76:79], v154, v154 op_sel_hi:[0,0,0]
	s_setprio 0
	s_barrier
	s_add_u32 s74, s0, 0x20080
	s_addc_u32 s75, s1, 0
	s_add_u32 s0, s0, 0x30080
	s_addc_u32 s1, s1, 0
	s_mov_b32 m0, s64
	s_nop 0
	v_lshl_add_u64 v[2:3], s[74:75], 0, v[252:253]
	global_load_lds_dwordx4 v[2:3], off
	v_lshl_add_u64 v[2:3], s[0:1], 0, v[252:253]
	s_mov_b32 m0, s65
	s_nop 0
	global_load_lds_dwordx4 v[2:3], off
	s_waitcnt vmcnt(6)
	s_barrier
	s_setprio 1
	v_mfma_scale_f32_16x16x128_f8f6f4 v[240:243], v[138:145], v[18:25], v[80:83], v154, v154 op_sel_hi:[0,0,0]
	v_mfma_scale_f32_16x16x128_f8f6f4 v[248:251], v[160:167], v[18:25], v[68:71], v154, v154 op_sel_hi:[0,0,0]
	v_mfma_scale_f32_16x16x128_f8f6f4 v[22:25], v[138:145], v[168:175], v[192:195], v154, v154 op_sel_hi:[0,0,0]
	v_mfma_scale_f32_16x16x128_f8f6f4 v[18:21], v[160:167], v[168:175], v[196:199], v154, v154 op_sel_hi:[0,0,0]
	v_mfma_scale_f32_16x16x128_f8f6f4 v[14:17], v[138:145], v[176:183], v[200:203], v154, v154 op_sel_hi:[0,0,0]
	v_mfma_scale_f32_16x16x128_f8f6f4 v[10:13], v[160:167], v[176:183], v[96:99], v154, v154 op_sel_hi:[0,0,0]
	v_mfma_scale_f32_16x16x128_f8f6f4 v[92:95], v[138:145], v[184:191], v[100:103], v154, v154 op_sel_hi:[0,0,0]
	s_nop 5
	v_mov_b64_e32 v[96:97], v[132:133]
	v_mov_b64_e32 v[98:99], v[134:135]
	v_mfma_scale_f32_16x16x128_f8f6f4 v[2:5], v[160:167], v[184:191], v[104:107], v154, v154 op_sel_hi:[0,0,0]
	s_setprio 0
	v_mov_b32_e32 v34, v0
	s_barrier
; #define LAS __attribute__((address_space(3)))
; #define lds lds_hidden(lds0)
;     __device__ __forceinline__ void operator()(const f32x4 (&acc)[2][2][4][2], const Unit& u, int wr, int wc, int fr, int fq, LAS unsigned char* lds, int par) const {
;         LAS const float* tb = (LAS const float*)(lds + EPI_OFF + par * 2048);
;         const int colu = wc * 32 + 8 * fq, col = u.pn * 128 + colu;
;         const f32x4 bg0 = *(LAS const f32x4*)(tb + colu), bg1 = *(LAS const f32x4*)(tb + colu + 4), bl0 = *(LAS const f32x4*)(tb + 128 + colu), bl1 = *(LAS const f32x4*)(tb + 128 + colu + 4);
;         const float sc = kf(1.f / (W8_SCALE * H28_SCALE * MX_SCALE)), lim = kf(7.f), ke = kf(-1.702f * 1.4426950408889634f), one = kf(1.f), as = kf(ACT8_SCALE);
;         const f32x2_t sc2 = (f32x2_t){sc, sc}, ke2 = (f32x2_t){ke, ke}, one2 = (f32x2_t){one, one}, as2 = (f32x2_t){as, as};
; #pragma unroll
;         for (int ai = 0; ai < 2; ++ai)
; #pragma unroll
;             for (int m = 0; m < 4; ++m) {
;                 const int r = u.rt * BM + ai * HALF + wr * 64 + m * 16 + fr;
;                 f32x2_t o[4];
; #pragma unroll
;                 for (int n = 0; n < 2; ++n)
; #pragma unroll
;                     for (int h = 0; h < 2; ++h) {
;                         const f32x4 bgv = n ? bg1 : bg0, blv = n ? bl1 : bl0;
;                         f32x2_t glu = (f32x2_t){acc[ai][0][m][n][2 * h], acc[ai][0][m][n][2 * h + 1]} * sc2 + (f32x2_t){bgv[2 * h], bgv[2 * h + 1]};
;                         f32x2_t lin = (f32x2_t){acc[ai][1][m][n][2 * h], acc[ai][1][m][n][2 * h + 1]} * sc2 + (f32x2_t){blv[2 * h], blv[2 * h + 1]};
;                         glu.x = fminf(glu.x, lim); glu.y = fminf(glu.y, lim);
;                         lin.x = __builtin_amdgcn_fmed3f(lin.x, -lim, lim); lin.y = __builtin_amdgcn_fmed3f(lin.y, -lim, lim);
;                         const f32x2_t t = glu * ke2;
;                         const f32x2_t d = (f32x2_t){__builtin_amdgcn_exp2f(t.x), __builtin_amdgcn_exp2f(t.y)} + one2;
;                         const f32x2_t rc = (f32x2_t){__builtin_amdgcn_rcpf(d.x), __builtin_amdgcn_rcpf(d.y)};
;                         o[n * 2 + h] = (glu * rc) * (lin * as2 + as2);
;                     }
;                 const int ro = u.rowbase + r;
;                 u32x2 w; w.x = cvt_pk4_fp8(o[0].x, o[0].y, o[1].x, o[1].y); w.y = cvt_pk4_fp8(o[2].x, o[2].y, o[3].x, o[3].y);
	s_lshl_b32 s0, s68, 11
	v_readfirstlane_b32 s17, v34
	s_lshr_b32 s1, s17, 1
	s_and_b32 s1, s1, 0x60
	v_lshrrev_b32_e32 v68, 1, v34
	s_add_i32 s0, s67, s0
	v_and_or_b32 v69, v68, 24, s1
	v_lshl_or_b32 v68, s18, 7, v69
	v_lshl_add_u32 v69, v69, 2, s0
	ds_read_b128 v[140:143], v69
	ds_read_b128 v[132:135], v69 offset:16
	ds_read_b128 v[144:147], v69 offset:512
	ds_read_b128 v[136:139], v69 offset:528
	s_ashr_i32 s17, s17, 2
	s_mov_b32 s34, 0x3b000000
	s_mov_b32 s1, 0x40e00000
	s_mov_b32 s94, 0x39124925
	s_mov_b32 s95, 0x3d924925
	s_andn2_b32 s17, s17, 63
	v_ashrrev_i32_e32 v69, 31, v68
	v_and_or_b32 v80, v34, 15, s17
	v_lshl_add_u64 v[150:151], s[14:15], 0, v[68:69]
	s_waitcnt lgkmcnt(0)
	v_fma_f32 v144, v144, s95, 0.5
	v_fma_f32 v145, v145, s95, 0.5
	v_fma_f32 v146, v146, s95, 0.5
	v_fma_f32 v147, v147, s95, 0.5
	v_fma_f32 v136, v136, s95, 0.5
	v_fma_f32 v137, v137, s95, 0.5
	v_fma_f32 v138, v138, s95, 0.5
	v_fma_f32 v139, v139, s95, 0.5
	v_pk_fma_f32 v[68:69], v[128:129], s[34:35], v[140:141] op_sel_hi:[1,0,1]
	v_max_f32_e64 v34, s1, s1
	s_mov_b32 s1, 0xc1c00000
	s_mov_b32 s30, 0xc01d265f
	v_min_f32_e32 v68, v68, v34
	v_min_f32_e32 v69, v69, v34
	s_mov_b32 s2, 1.0
	v_pk_mul_f32 v[72:73], s[30:31], v[68:69] op_sel_hi:[0,1]
	v_exp_f32_e32 v72, v72
	v_exp_f32_e32 v73, v73
	v_pk_fma_f32 v[70:71], v[96:97], s[94:95], v[144:145] op_sel_hi:[1,0,1] clamp
	s_mov_b32 s0, 0x42600000
	v_pk_add_f32 v[72:73], s[2:3], v[72:73] op_sel_hi:[0,1]
	v_rcp_f32_e32 v72, v72
	v_rcp_f32_e32 v73, v73
	s_nop 0
	v_pk_mul_f32 v[68:69], v[68:69], v[72:73]
	v_pk_fma_f32 v[70:71], s[0:1], v[70:71], s[0:1] op_sel:[0,0,1] op_sel_hi:[0,1,1]
	v_pk_mul_f32 v[68:69], v[70:71], v[68:69]
	v_pk_fma_f32 v[70:71], v[130:131], s[34:35], v[142:143] op_sel_hi:[1,0,1]
	v_pk_fma_f32 v[72:73], v[98:99], s[94:95], v[146:147] op_sel_hi:[1,0,1] clamp
	v_min_f32_e32 v70, v70, v34
	v_min_f32_e32 v71, v71, v34
	v_pk_mul_f32 v[74:75], s[30:31], v[70:71] op_sel_hi:[0,1]
	v_exp_f32_e32 v74, v74
	v_exp_f32_e32 v75, v75
	v_pk_fma_f32 v[72:73], s[0:1], v[72:73], s[0:1] op_sel:[0,0,1] op_sel_hi:[0,1,1]
	v_pk_add_f32 v[74:75], s[2:3], v[74:75] op_sel_hi:[0,1]
	v_rcp_f32_e32 v74, v74
	v_rcp_f32_e32 v75, v75
	s_lshl_b32 s17, s38, 8
	s_add_i32 s17, s17, s39
	v_add_u32_e32 v152, s17, v80
	v_pk_mul_f32 v[70:71], v[70:71], v[74:75]
	v_pk_fma_f32 v[74:75], v[84:85], s[94:95], v[136:137] op_sel_hi:[1,0,1] clamp
	v_pk_mul_f32 v[70:71], v[72:73], v[70:71]
	v_pk_fma_f32 v[72:73], v[124:125], s[34:35], v[132:133] op_sel_hi:[1,0,1]
	v_min_f32_e32 v72, v72, v34
	v_min_f32_e32 v73, v73, v34
	v_pk_mul_f32 v[76:77], s[30:31], v[72:73] op_sel_hi:[0,1]
	v_exp_f32_e32 v76, v76
	v_exp_f32_e32 v77, v77
	v_pk_fma_f32 v[74:75], s[0:1], v[74:75], s[0:1] op_sel:[0,0,1] op_sel_hi:[0,1,1]
	v_ashrrev_i32_e32 v153, 31, v152
	v_pk_add_f32 v[76:77], s[2:3], v[76:77] op_sel_hi:[0,1]
	v_rcp_f32_e32 v76, v76
	v_rcp_f32_e32 v77, v77
	v_mov_b64_e32 v[80:81], v[208:209]
	v_mov_b64_e32 v[82:83], v[210:211]
	s_and_b64 vcc, exec, s[4:5]
	v_pk_mul_f32 v[72:73], v[72:73], v[76:77]
	v_pk_fma_f32 v[76:77], v[86:87], s[94:95], v[138:139] op_sel_hi:[1,0,1] clamp
	v_pk_mul_f32 v[72:73], v[74:75], v[72:73]
	v_pk_fma_f32 v[74:75], v[126:127], s[34:35], v[134:135] op_sel_hi:[1,0,1]
	v_min_f32_e32 v74, v74, v34
	v_min_f32_e32 v75, v75, v34
	v_pk_mul_f32 v[78:79], s[30:31], v[74:75] op_sel_hi:[0,1]
	v_exp_f32_e32 v78, v78
	v_exp_f32_e32 v79, v79
	v_pk_fma_f32 v[76:77], s[0:1], v[76:77], s[0:1] op_sel:[0,0,1] op_sel_hi:[0,1,1]
	v_pk_add_f32 v[78:79], s[2:3], v[78:79] op_sel_hi:[0,1]
	v_rcp_f32_e32 v78, v78
	v_rcp_f32_e32 v79, v79
	s_nop 0
	v_pk_mul_f32 v[74:75], v[74:75], v[78:79]
	s_nop 0
	v_pk_mul_f32 v[74:75], v[76:77], v[74:75]
	v_mov_b32_e32 v76, v35
	v_mov_b32_e32 v77, v35
	v_cvt_pk_fp8_f32 v76, v68, v69
	v_cvt_pk_fp8_f32 v77, v72, v73
	v_lshlrev_b64 v[68:69], 10, v[152:153]
	v_lshl_add_u64 v[68:69], v[150:151], 0, v[68:69]
	v_cvt_pk_fp8_f32 v76, v70, v71 op_sel:[0,0,1]
	v_cvt_pk_fp8_f32 v77, v74, v75 op_sel:[0,0,1]
	v_pk_fma_f32 v[70:71], v[88:89], s[94:95], v[144:145] op_sel_hi:[1,0,1] clamp
	global_store_dwordx2 v[68:69], v[76:77], off sc1
	v_pk_fma_f32 v[68:69], v[120:121], s[34:35], v[140:141] op_sel_hi:[1,0,1]
	v_min_f32_e32 v68, v68, v34
	v_min_f32_e32 v69, v69, v34
	v_pk_mul_f32 v[72:73], s[30:31], v[68:69] op_sel_hi:[0,1]
	v_exp_f32_e32 v72, v72
	v_exp_f32_e32 v73, v73
	v_pk_fma_f32 v[70:71], s[0:1], v[70:71], s[0:1] op_sel:[0,0,1] op_sel_hi:[0,1,1]
	v_pk_add_f32 v[72:73], s[2:3], v[72:73] op_sel_hi:[0,1]
	v_rcp_f32_e32 v72, v72
	v_rcp_f32_e32 v73, v73
	s_nop 0
	v_pk_mul_f32 v[68:69], v[68:69], v[72:73]
	s_nop 0
	v_pk_mul_f32 v[68:69], v[70:71], v[68:69]
	v_pk_fma_f32 v[70:71], v[122:123], s[34:35], v[142:143] op_sel_hi:[1,0,1]
	v_pk_fma_f32 v[72:73], v[90:91], s[94:95], v[146:147] op_sel_hi:[1,0,1] clamp
	v_min_f32_e32 v70, v70, v34
	v_min_f32_e32 v71, v71, v34
	v_pk_mul_f32 v[74:75], s[30:31], v[70:71] op_sel_hi:[0,1]
	v_exp_f32_e32 v74, v74
	v_exp_f32_e32 v75, v75
	v_pk_fma_f32 v[72:73], s[0:1], v[72:73], s[0:1] op_sel:[0,0,1] op_sel_hi:[0,1,1]
	v_pk_add_f32 v[74:75], s[2:3], v[74:75] op_sel_hi:[0,1]
	v_rcp_f32_e32 v74, v74
	v_rcp_f32_e32 v75, v75
	s_nop 0
	v_pk_mul_f32 v[70:71], v[70:71], v[74:75]
	s_nop 0
	v_pk_mul_f32 v[70:71], v[72:73], v[70:71]
	v_pk_fma_f32 v[72:73], v[116:117], s[34:35], v[132:133] op_sel_hi:[1,0,1]
	v_pk_fma_f32 v[74:75], v[26:27], s[94:95], v[136:137] op_sel_hi:[1,0,1] clamp
	v_min_f32_e32 v72, v72, v34
	v_min_f32_e32 v73, v73, v34
	v_pk_mul_f32 v[76:77], s[30:31], v[72:73] op_sel_hi:[0,1]
	v_exp_f32_e32 v76, v76
	v_exp_f32_e32 v77, v77
	v_pk_fma_f32 v[74:75], s[0:1], v[74:75], s[0:1] op_sel:[0,0,1] op_sel_hi:[0,1,1]
; __device__ __forceinline__ unsigned cvt_pk4_fp8(float a, float b, float c, float d) { int w = 0; w = __builtin_amdgcn_cvt_pk_fp8_f32(a, b, w, false); w = __builtin_amdgcn_cvt_pk_fp8_f32(c, d, w, true); return (unsigned)w; }
; #define GAS __attribute__((address_space(1)))
;     __device__ __forceinline__ void operator()(const f32x4 (&acc)[2][2][4][2], const Unit& u, int wr, int wc, int fr, int fq, LAS unsigned char* lds, int par) const {
;     ...
;         for (int ai = 0; ai < 2; ++ai)
; #pragma unroll
;             for (int m = 0; m < 4; ++m) {
;                 const int r = u.rt * BM + ai * HALF + wr * 64 + m * 16 + fr;
;                 f32x2_t o[4];
; #pragma unroll
;                 for (int n = 0; n < 2; ++n)
; #pragma unroll
;                     for (int h = 0; h < 2; ++h) {
;                         const f32x4 bgv = n ? bg1 : bg0, blv = n ? bl1 : bl0;
;                         f32x2_t glu = (f32x2_t){acc[ai][0][m][n][2 * h], acc[ai][0][m][n][2 * h + 1]} * sc2 + (f32x2_t){bgv[2 * h], bgv[2 * h + 1]};
;                         f32x2_t lin = (f32x2_t){acc[ai][1][m][n][2 * h], acc[ai][1][m][n][2 * h + 1]} * sc2 + (f32x2_t){blv[2 * h], blv[2 * h + 1]};
;                         glu.x = fminf(glu.x, lim); glu.y = fminf(glu.y, lim);
;                         lin.x = __builtin_amdgcn_fmed3f(lin.x, -lim, lim); lin.y = __builtin_amdgcn_fmed3f(lin.y, -lim, lim);
;                         const f32x2_t t = glu * ke2;
;                         const f32x2_t d = (f32x2_t){__builtin_amdgcn_exp2f(t.x), __builtin_amdgcn_exp2f(t.y)} + one2;
;                         const f32x2_t rc = (f32x2_t){__builtin_amdgcn_rcpf(d.x), __builtin_amdgcn_rcpf(d.y)};
;                         o[n * 2 + h] = (glu * rc) * (lin * as2 + as2);
;                     }
;                 const int ro = u.rowbase + r;
;                 u32x2 w; w.x = cvt_pk4_fp8(o[0].x, o[0].y, o[1].x, o[1].y); w.y = cvt_pk4_fp8(o[2].x, o[2].y, o[3].x, o[3].y);
;                 __hip_atomic_store((unsigned long long GAS*)(act + (size_t)ro * DFF + col), ((unsigned long long)w.y << 32) | w.x, __ATOMIC_RELAXED, __HIP_MEMORY_SCOPE_AGENT);
	v_pk_add_f32 v[76:77], s[2:3], v[76:77] op_sel_hi:[0,1]
	v_rcp_f32_e32 v76, v76
	v_rcp_f32_e32 v77, v77
	s_nop 0
	v_pk_mul_f32 v[72:73], v[72:73], v[76:77]
	s_nop 0
	v_pk_mul_f32 v[72:73], v[74:75], v[72:73]
	v_pk_fma_f32 v[74:75], v[118:119], s[34:35], v[134:135] op_sel_hi:[1,0,1]
	v_pk_fma_f32 v[76:77], v[28:29], s[94:95], v[138:139] op_sel_hi:[1,0,1] clamp
	v_min_f32_e32 v74, v74, v34
	v_min_f32_e32 v75, v75, v34
	v_pk_mul_f32 v[78:79], s[30:31], v[74:75] op_sel_hi:[0,1]
	v_exp_f32_e32 v78, v78
	v_exp_f32_e32 v79, v79
	v_pk_fma_f32 v[76:77], s[0:1], v[76:77], s[0:1] op_sel:[0,0,1] op_sel_hi:[0,1,1]
	v_pk_add_f32 v[78:79], s[2:3], v[78:79] op_sel_hi:[0,1]
	v_rcp_f32_e32 v78, v78
	v_rcp_f32_e32 v79, v79
	s_nop 0
	v_pk_mul_f32 v[74:75], v[74:75], v[78:79]
	v_mov_b32_e32 v78, v35
	v_mov_b32_e32 v79, v35
	v_cvt_pk_fp8_f32 v78, v68, v69
	v_cvt_pk_fp8_f32 v79, v72, v73
	v_pk_mul_f32 v[74:75], v[76:77], v[74:75]
	v_add_u32_e32 v76, 16, v152
	v_cvt_pk_fp8_f32 v78, v70, v71 op_sel:[0,0,1]
	v_cvt_pk_fp8_f32 v79, v74, v75 op_sel:[0,0,1]
	v_ashrrev_i32_e32 v77, 31, v76
	v_lshlrev_b64 v[68:69], 10, v[76:77]
	v_lshl_add_u64 v[68:69], v[150:151], 0, v[68:69]
	global_store_dwordx2 v[68:69], v[78:79], off sc1
	v_pk_fma_f32 v[68:69], v[112:113], s[34:35], v[140:141] op_sel_hi:[1,0,1]
	v_pk_fma_f32 v[70:71], v[52:53], s[94:95], v[144:145] op_sel_hi:[1,0,1] clamp
	v_min_f32_e32 v68, v68, v34
	v_min_f32_e32 v69, v69, v34
	v_pk_mul_f32 v[72:73], s[30:31], v[68:69] op_sel_hi:[0,1]
	v_exp_f32_e32 v72, v72
	v_exp_f32_e32 v73, v73
	v_pk_fma_f32 v[70:71], s[0:1], v[70:71], s[0:1] op_sel:[0,0,1] op_sel_hi:[0,1,1]
	v_pk_add_f32 v[72:73], s[2:3], v[72:73] op_sel_hi:[0,1]
	v_rcp_f32_e32 v72, v72
	v_rcp_f32_e32 v73, v73
	s_nop 0
	v_pk_mul_f32 v[68:69], v[68:69], v[72:73]
	s_nop 0
	v_pk_mul_f32 v[68:69], v[70:71], v[68:69]
	v_pk_fma_f32 v[70:71], v[114:115], s[34:35], v[142:143] op_sel_hi:[1,0,1]
	v_pk_fma_f32 v[72:73], v[54:55], s[94:95], v[146:147] op_sel_hi:[1,0,1] clamp
	v_min_f32_e32 v70, v70, v34
	v_min_f32_e32 v71, v71, v34
	v_pk_mul_f32 v[74:75], s[30:31], v[70:71] op_sel_hi:[0,1]
	v_exp_f32_e32 v74, v74
	v_exp_f32_e32 v75, v75
	v_pk_fma_f32 v[72:73], s[0:1], v[72:73], s[0:1] op_sel:[0,0,1] op_sel_hi:[0,1,1]
	v_pk_add_f32 v[74:75], s[2:3], v[74:75] op_sel_hi:[0,1]
	v_rcp_f32_e32 v74, v74
	v_rcp_f32_e32 v75, v75
	s_nop 0
	v_pk_mul_f32 v[70:71], v[70:71], v[74:75]
	s_nop 0
	v_pk_mul_f32 v[70:71], v[72:73], v[70:71]
	v_pk_fma_f32 v[72:73], v[108:109], s[34:35], v[132:133] op_sel_hi:[1,0,1]
	v_pk_fma_f32 v[74:75], v[36:37], s[94:95], v[136:137] op_sel_hi:[1,0,1] clamp
	v_min_f32_e32 v72, v72, v34
	v_min_f32_e32 v73, v73, v34
	v_pk_mul_f32 v[76:77], s[30:31], v[72:73] op_sel_hi:[0,1]
	v_exp_f32_e32 v76, v76
	v_exp_f32_e32 v77, v77
	v_pk_fma_f32 v[74:75], s[0:1], v[74:75], s[0:1] op_sel:[0,0,1] op_sel_hi:[0,1,1]
	v_pk_add_f32 v[76:77], s[2:3], v[76:77] op_sel_hi:[0,1]
	v_rcp_f32_e32 v76, v76
	v_rcp_f32_e32 v77, v77
	s_nop 0
	v_pk_mul_f32 v[72:73], v[72:73], v[76:77]
	s_nop 0
	v_pk_mul_f32 v[72:73], v[74:75], v[72:73]
	v_pk_fma_f32 v[74:75], v[110:111], s[34:35], v[134:135] op_sel_hi:[1,0,1]
	v_pk_fma_f32 v[76:77], v[38:39], s[94:95], v[138:139] op_sel_hi:[1,0,1] clamp
	v_min_f32_e32 v74, v74, v34
	v_min_f32_e32 v75, v75, v34
	v_pk_mul_f32 v[78:79], s[30:31], v[74:75] op_sel_hi:[0,1]
	v_exp_f32_e32 v78, v78
	v_exp_f32_e32 v79, v79
	v_pk_fma_f32 v[76:77], s[0:1], v[76:77], s[0:1] op_sel:[0,0,1] op_sel_hi:[0,1,1]
	v_pk_add_f32 v[78:79], s[2:3], v[78:79] op_sel_hi:[0,1]
	v_rcp_f32_e32 v78, v78
	v_rcp_f32_e32 v79, v79
	s_nop 0
	v_pk_mul_f32 v[74:75], v[74:75], v[78:79]
	v_mov_b32_e32 v78, v35
	v_mov_b32_e32 v79, v35
	v_cvt_pk_fp8_f32 v78, v68, v69
	v_cvt_pk_fp8_f32 v79, v72, v73
	v_pk_mul_f32 v[74:75], v[76:77], v[74:75]
	v_add_u32_e32 v76, 32, v152
	v_cvt_pk_fp8_f32 v78, v70, v71 op_sel:[0,0,1]
	v_cvt_pk_fp8_f32 v79, v74, v75 op_sel:[0,0,1]
	v_ashrrev_i32_e32 v77, 31, v76
	v_lshlrev_b64 v[68:69], 10, v[76:77]
	v_lshl_add_u64 v[68:69], v[150:151], 0, v[68:69]
	global_store_dwordx2 v[68:69], v[78:79], off sc1
	v_pk_fma_f32 v[68:69], v[204:205], s[34:35], v[140:141] op_sel_hi:[1,0,1]
	v_pk_fma_f32 v[70:71], v[30:31], s[94:95], v[144:145] op_sel_hi:[1,0,1] clamp
	v_min_f32_e32 v68, v68, v34
	v_min_f32_e32 v69, v69, v34
	v_pk_mul_f32 v[72:73], s[30:31], v[68:69] op_sel_hi:[0,1]
	v_exp_f32_e32 v72, v72
	v_exp_f32_e32 v73, v73
	v_pk_fma_f32 v[70:71], s[0:1], v[70:71], s[0:1] op_sel:[0,0,1] op_sel_hi:[0,1,1]
	v_pk_add_f32 v[72:73], s[2:3], v[72:73] op_sel_hi:[0,1]
	v_rcp_f32_e32 v72, v72
	v_rcp_f32_e32 v73, v73
	s_nop 0
	v_pk_mul_f32 v[68:69], v[68:69], v[72:73]
	s_nop 0
	v_pk_mul_f32 v[68:69], v[70:71], v[68:69]
	v_pk_fma_f32 v[70:71], v[206:207], s[34:35], v[142:143] op_sel_hi:[1,0,1]
	v_pk_fma_f32 v[72:73], v[32:33], s[94:95], v[146:147] op_sel_hi:[1,0,1] clamp
	v_min_f32_e32 v70, v70, v34
	v_min_f32_e32 v71, v71, v34
	v_pk_mul_f32 v[74:75], s[30:31], v[70:71] op_sel_hi:[0,1]
	v_exp_f32_e32 v74, v74
	v_exp_f32_e32 v75, v75
	v_pk_fma_f32 v[72:73], s[0:1], v[72:73], s[0:1] op_sel:[0,0,1] op_sel_hi:[0,1,1]
	v_pk_add_f32 v[74:75], s[2:3], v[74:75] op_sel_hi:[0,1]
	v_rcp_f32_e32 v74, v74
	v_rcp_f32_e32 v75, v75
	s_nop 0
	v_pk_mul_f32 v[70:71], v[70:71], v[74:75]
	s_nop 0
	v_pk_mul_f32 v[70:71], v[72:73], v[70:71]
	v_pk_fma_f32 v[72:73], v[80:81], s[34:35], v[132:133] op_sel_hi:[1,0,1]
	v_pk_fma_f32 v[74:75], v[40:41], s[94:95], v[136:137] op_sel_hi:[1,0,1] clamp
	v_min_f32_e32 v72, v72, v34
	v_min_f32_e32 v73, v73, v34
	v_pk_mul_f32 v[76:77], s[30:31], v[72:73] op_sel_hi:[0,1]
	v_exp_f32_e32 v76, v76
	v_exp_f32_e32 v77, v77
	v_pk_fma_f32 v[74:75], s[0:1], v[74:75], s[0:1] op_sel:[0,0,1] op_sel_hi:[0,1,1]
; __device__ __forceinline__ unsigned cvt_pk4_fp8(float a, float b, float c, float d) { int w = 0; w = __builtin_amdgcn_cvt_pk_fp8_f32(a, b, w, false); w = __builtin_amdgcn_cvt_pk_fp8_f32(c, d, w, true); return (unsigned)w; }
; #define GAS __attribute__((address_space(1)))
;     __device__ __forceinline__ void operator()(const f32x4 (&acc)[2][2][4][2], const Unit& u, int wr, int wc, int fr, int fq, LAS unsigned char* lds, int par) const {
;     ...
;         for (int ai = 0; ai < 2; ++ai)
; #pragma unroll
;             for (int m = 0; m < 4; ++m) {
;                 const int r = u.rt * BM + ai * HALF + wr * 64 + m * 16 + fr;
;                 f32x2_t o[4];
; #pragma unroll
;                 for (int n = 0; n < 2; ++n)
; #pragma unroll
;                     for (int h = 0; h < 2; ++h) {
;                         const f32x4 bgv = n ? bg1 : bg0, blv = n ? bl1 : bl0;
;                         f32x2_t glu = (f32x2_t){acc[ai][0][m][n][2 * h], acc[ai][0][m][n][2 * h + 1]} * sc2 + (f32x2_t){bgv[2 * h], bgv[2 * h + 1]};
;                         f32x2_t lin = (f32x2_t){acc[ai][1][m][n][2 * h], acc[ai][1][m][n][2 * h + 1]} * sc2 + (f32x2_t){blv[2 * h], blv[2 * h + 1]};
;                         glu.x = fminf(glu.x, lim); glu.y = fminf(glu.y, lim);
;                         lin.x = __builtin_amdgcn_fmed3f(lin.x, -lim, lim); lin.y = __builtin_amdgcn_fmed3f(lin.y, -lim, lim);
;                         const f32x2_t t = glu * ke2;
;                         const f32x2_t d = (f32x2_t){__builtin_amdgcn_exp2f(t.x), __builtin_amdgcn_exp2f(t.y)} + one2;
;                         const f32x2_t rc = (f32x2_t){__builtin_amdgcn_rcpf(d.x), __builtin_amdgcn_rcpf(d.y)};
;                         o[n * 2 + h] = (glu * rc) * (lin * as2 + as2);
;                     }
;                 const int ro = u.rowbase + r;
;                 u32x2 w; w.x = cvt_pk4_fp8(o[0].x, o[0].y, o[1].x, o[1].y); w.y = cvt_pk4_fp8(o[2].x, o[2].y, o[3].x, o[3].y);
;                 __hip_atomic_store((unsigned long long GAS*)(act + (size_t)ro * DFF + col), ((unsigned long long)w.y << 32) | w.x, __ATOMIC_RELAXED, __HIP_MEMORY_SCOPE_AGENT);
	v_pk_add_f32 v[76:77], s[2:3], v[76:77] op_sel_hi:[0,1]
	v_rcp_f32_e32 v76, v76
	v_rcp_f32_e32 v77, v77
	s_nop 0
	v_pk_mul_f32 v[72:73], v[72:73], v[76:77]
	s_nop 0
	v_pk_mul_f32 v[72:73], v[74:75], v[72:73]
	v_pk_fma_f32 v[74:75], v[82:83], s[34:35], v[134:135] op_sel_hi:[1,0,1]
	v_pk_fma_f32 v[76:77], v[42:43], s[94:95], v[138:139] op_sel_hi:[1,0,1] clamp
	v_min_f32_e32 v74, v74, v34
	v_min_f32_e32 v75, v75, v34
	v_pk_mul_f32 v[78:79], s[30:31], v[74:75] op_sel_hi:[0,1]
	v_exp_f32_e32 v78, v78
	v_exp_f32_e32 v79, v79
	v_pk_fma_f32 v[76:77], s[0:1], v[76:77], s[0:1] op_sel:[0,0,1] op_sel_hi:[0,1,1]
	v_pk_add_f32 v[78:79], s[2:3], v[78:79] op_sel_hi:[0,1]
	v_rcp_f32_e32 v78, v78
	v_rcp_f32_e32 v79, v79
	s_nop 0
	v_pk_mul_f32 v[74:75], v[74:75], v[78:79]
	v_mov_b32_e32 v78, v35
	v_mov_b32_e32 v79, v35
	v_cvt_pk_fp8_f32 v78, v68, v69
	v_cvt_pk_fp8_f32 v79, v72, v73
	v_pk_mul_f32 v[74:75], v[76:77], v[74:75]
	v_add_u32_e32 v76, 48, v152
	v_cvt_pk_fp8_f32 v78, v70, v71 op_sel:[0,0,1]
	v_cvt_pk_fp8_f32 v79, v74, v75 op_sel:[0,0,1]
	v_ashrrev_i32_e32 v77, 31, v76
	v_lshlrev_b64 v[68:69], 10, v[76:77]
	v_lshl_add_u64 v[68:69], v[150:151], 0, v[68:69]
	global_store_dwordx2 v[68:69], v[78:79], off sc1
	v_pk_fma_f32 v[68:69], v[64:65], s[34:35], v[140:141] op_sel_hi:[1,0,1]
	v_pk_fma_f32 v[70:71], v[240:241], s[94:95], v[144:145] op_sel_hi:[1,0,1] clamp
	v_min_f32_e32 v68, v68, v34
	v_min_f32_e32 v69, v69, v34
	v_pk_mul_f32 v[72:73], s[30:31], v[68:69] op_sel_hi:[0,1]
	v_exp_f32_e32 v72, v72
	v_exp_f32_e32 v73, v73
	v_pk_fma_f32 v[70:71], s[0:1], v[70:71], s[0:1] op_sel:[0,0,1] op_sel_hi:[0,1,1]
	v_pk_add_f32 v[72:73], s[2:3], v[72:73] op_sel_hi:[0,1]
	v_rcp_f32_e32 v72, v72
	v_rcp_f32_e32 v73, v73
	s_nop 0
	v_pk_mul_f32 v[68:69], v[68:69], v[72:73]
	s_nop 0
	v_pk_mul_f32 v[68:69], v[70:71], v[68:69]
	v_pk_fma_f32 v[70:71], v[66:67], s[34:35], v[142:143] op_sel_hi:[1,0,1]
	v_pk_fma_f32 v[72:73], v[242:243], s[94:95], v[146:147] op_sel_hi:[1,0,1] clamp
	v_min_f32_e32 v70, v70, v34
	v_min_f32_e32 v71, v71, v34
	v_pk_mul_f32 v[74:75], s[30:31], v[70:71] op_sel_hi:[0,1]
	v_exp_f32_e32 v74, v74
	v_exp_f32_e32 v75, v75
	v_pk_fma_f32 v[72:73], s[0:1], v[72:73], s[0:1] op_sel:[0,0,1] op_sel_hi:[0,1,1]
	v_pk_add_f32 v[74:75], s[2:3], v[74:75] op_sel_hi:[0,1]
	v_rcp_f32_e32 v74, v74
	v_rcp_f32_e32 v75, v75
	s_nop 0
	v_pk_mul_f32 v[70:71], v[70:71], v[74:75]
	s_nop 0
	v_pk_mul_f32 v[70:71], v[72:73], v[70:71]
	v_pk_fma_f32 v[72:73], v[60:61], s[34:35], v[132:133] op_sel_hi:[1,0,1]
	v_pk_fma_f32 v[74:75], v[248:249], s[94:95], v[136:137] op_sel_hi:[1,0,1] clamp
	v_min_f32_e32 v72, v72, v34
	v_min_f32_e32 v73, v73, v34
	v_pk_mul_f32 v[76:77], s[30:31], v[72:73] op_sel_hi:[0,1]
	v_exp_f32_e32 v76, v76
	v_exp_f32_e32 v77, v77
	v_pk_fma_f32 v[74:75], s[0:1], v[74:75], s[0:1] op_sel:[0,0,1] op_sel_hi:[0,1,1]
	v_pk_add_f32 v[76:77], s[2:3], v[76:77] op_sel_hi:[0,1]
	v_rcp_f32_e32 v76, v76
	v_rcp_f32_e32 v77, v77
	s_nop 0
	v_pk_mul_f32 v[72:73], v[72:73], v[76:77]
	s_nop 0
	v_pk_mul_f32 v[72:73], v[74:75], v[72:73]
	v_pk_fma_f32 v[74:75], v[62:63], s[34:35], v[134:135] op_sel_hi:[1,0,1]
	v_pk_fma_f32 v[76:77], v[250:251], s[94:95], v[138:139] op_sel_hi:[1,0,1] clamp
	v_min_f32_e32 v74, v74, v34
	v_min_f32_e32 v75, v75, v34
	v_pk_mul_f32 v[78:79], s[30:31], v[74:75] op_sel_hi:[0,1]
	v_exp_f32_e32 v78, v78
	v_exp_f32_e32 v79, v79
	v_pk_fma_f32 v[76:77], s[0:1], v[76:77], s[0:1] op_sel:[0,0,1] op_sel_hi:[0,1,1]
	v_pk_add_f32 v[78:79], s[2:3], v[78:79] op_sel_hi:[0,1]
	v_rcp_f32_e32 v78, v78
	v_rcp_f32_e32 v79, v79
	s_nop 0
	v_pk_mul_f32 v[74:75], v[74:75], v[78:79]
	v_mov_b32_e32 v78, v35
	v_mov_b32_e32 v79, v35
	v_cvt_pk_fp8_f32 v78, v68, v69
	v_cvt_pk_fp8_f32 v79, v72, v73
	v_pk_mul_f32 v[74:75], v[76:77], v[74:75]
	v_add_u32_e32 v76, 0x80, v152
	v_cvt_pk_fp8_f32 v78, v70, v71 op_sel:[0,0,1]
	v_cvt_pk_fp8_f32 v79, v74, v75 op_sel:[0,0,1]
	v_ashrrev_i32_e32 v77, 31, v76
	v_lshlrev_b64 v[68:69], 10, v[76:77]
	v_lshl_add_u64 v[68:69], v[150:151], 0, v[68:69]
	global_store_dwordx2 v[68:69], v[78:79], off sc1
	v_pk_fma_f32 v[68:69], v[56:57], s[34:35], v[140:141] op_sel_hi:[1,0,1]
	v_pk_fma_f32 v[70:71], v[22:23], s[94:95], v[144:145] op_sel_hi:[1,0,1] clamp
	v_min_f32_e32 v68, v68, v34
	v_min_f32_e32 v69, v69, v34
	v_pk_mul_f32 v[72:73], s[30:31], v[68:69] op_sel_hi:[0,1]
	v_exp_f32_e32 v72, v72
	v_exp_f32_e32 v73, v73
	v_pk_fma_f32 v[70:71], s[0:1], v[70:71], s[0:1] op_sel:[0,0,1] op_sel_hi:[0,1,1]
	v_pk_add_f32 v[72:73], s[2:3], v[72:73] op_sel_hi:[0,1]
	v_rcp_f32_e32 v72, v72
	v_rcp_f32_e32 v73, v73
	s_nop 0
	v_pk_mul_f32 v[68:69], v[68:69], v[72:73]
	s_nop 0
	v_pk_mul_f32 v[68:69], v[70:71], v[68:69]
	v_pk_fma_f32 v[70:71], v[58:59], s[34:35], v[142:143] op_sel_hi:[1,0,1]
	v_pk_fma_f32 v[72:73], v[24:25], s[94:95], v[146:147] op_sel_hi:[1,0,1] clamp
	v_min_f32_e32 v70, v70, v34
	v_min_f32_e32 v71, v71, v34
	v_pk_mul_f32 v[74:75], s[30:31], v[70:71] op_sel_hi:[0,1]
	v_exp_f32_e32 v74, v74
	v_exp_f32_e32 v75, v75
	v_pk_fma_f32 v[72:73], s[0:1], v[72:73], s[0:1] op_sel:[0,0,1] op_sel_hi:[0,1,1]
	v_pk_add_f32 v[74:75], s[2:3], v[74:75] op_sel_hi:[0,1]
	v_rcp_f32_e32 v74, v74
	v_rcp_f32_e32 v75, v75
	s_nop 0
	v_pk_mul_f32 v[70:71], v[70:71], v[74:75]
	s_nop 0
	v_pk_mul_f32 v[70:71], v[72:73], v[70:71]
	v_pk_fma_f32 v[72:73], v[236:237], s[34:35], v[132:133] op_sel_hi:[1,0,1]
	v_pk_fma_f32 v[74:75], v[18:19], s[94:95], v[136:137] op_sel_hi:[1,0,1] clamp
	v_min_f32_e32 v72, v72, v34
	v_min_f32_e32 v73, v73, v34
	v_pk_mul_f32 v[76:77], s[30:31], v[72:73] op_sel_hi:[0,1]
	v_exp_f32_e32 v76, v76
	v_exp_f32_e32 v77, v77
	v_pk_fma_f32 v[74:75], s[0:1], v[74:75], s[0:1] op_sel:[0,0,1] op_sel_hi:[0,1,1]
; __device__ __forceinline__ unsigned cvt_pk4_fp8(float a, float b, float c, float d) { int w = 0; w = __builtin_amdgcn_cvt_pk_fp8_f32(a, b, w, false); w = __builtin_amdgcn_cvt_pk_fp8_f32(c, d, w, true); return (unsigned)w; }
; #define GAS __attribute__((address_space(1)))
; template <class Epi, class Src>
; __device__ __forceinline__ void gemm_phase(LAS unsigned char* lds, const Src S, const Epi E) {
;     ...
;         if (!has_next) break;
;     __device__ __forceinline__ void operator()(const f32x4 (&acc)[2][2][4][2], const Unit& u, int wr, int wc, int fr, int fq, LAS unsigned char* lds, int par) const {
;     ...
;         for (int ai = 0; ai < 2; ++ai)
; #pragma unroll
;             for (int m = 0; m < 4; ++m) {
;                 const int r = u.rt * BM + ai * HALF + wr * 64 + m * 16 + fr;
;                 f32x2_t o[4];
; #pragma unroll
;                 for (int n = 0; n < 2; ++n)
; #pragma unroll
;                     for (int h = 0; h < 2; ++h) {
;                         const f32x4 bgv = n ? bg1 : bg0, blv = n ? bl1 : bl0;
;                         f32x2_t glu = (f32x2_t){acc[ai][0][m][n][2 * h], acc[ai][0][m][n][2 * h + 1]} * sc2 + (f32x2_t){bgv[2 * h], bgv[2 * h + 1]};
;                         f32x2_t lin = (f32x2_t){acc[ai][1][m][n][2 * h], acc[ai][1][m][n][2 * h + 1]} * sc2 + (f32x2_t){blv[2 * h], blv[2 * h + 1]};
;                         glu.x = fminf(glu.x, lim); glu.y = fminf(glu.y, lim);
;                         lin.x = __builtin_amdgcn_fmed3f(lin.x, -lim, lim); lin.y = __builtin_amdgcn_fmed3f(lin.y, -lim, lim);
;                         const f32x2_t t = glu * ke2;
;                         const f32x2_t d = (f32x2_t){__builtin_amdgcn_exp2f(t.x), __builtin_amdgcn_exp2f(t.y)} + one2;
;                         const f32x2_t rc = (f32x2_t){__builtin_amdgcn_rcpf(d.x), __builtin_amdgcn_rcpf(d.y)};
;                         o[n * 2 + h] = (glu * rc) * (lin * as2 + as2);
;                     }
;                 const int ro = u.rowbase + r;
;                 u32x2 w; w.x = cvt_pk4_fp8(o[0].x, o[0].y, o[1].x, o[1].y); w.y = cvt_pk4_fp8(o[2].x, o[2].y, o[3].x, o[3].y);
;                 __hip_atomic_store((unsigned long long GAS*)(act + (size_t)ro * DFF + col), ((unsigned long long)w.y << 32) | w.x, __ATOMIC_RELAXED, __HIP_MEMORY_SCOPE_AGENT);
;             }
	v_pk_add_f32 v[76:77], s[2:3], v[76:77] op_sel_hi:[0,1]
	v_rcp_f32_e32 v76, v76
	v_rcp_f32_e32 v77, v77
	s_nop 0
	v_pk_mul_f32 v[72:73], v[72:73], v[76:77]
	s_nop 0
	v_pk_mul_f32 v[72:73], v[74:75], v[72:73]
	v_pk_fma_f32 v[74:75], v[238:239], s[34:35], v[134:135] op_sel_hi:[1,0,1]
	v_pk_fma_f32 v[76:77], v[20:21], s[94:95], v[138:139] op_sel_hi:[1,0,1] clamp
	v_min_f32_e32 v74, v74, v34
	v_min_f32_e32 v75, v75, v34
	v_pk_mul_f32 v[78:79], s[30:31], v[74:75] op_sel_hi:[0,1]
	v_exp_f32_e32 v78, v78
	v_exp_f32_e32 v79, v79
	v_pk_fma_f32 v[76:77], s[0:1], v[76:77], s[0:1] op_sel:[0,0,1] op_sel_hi:[0,1,1]
	v_pk_add_f32 v[78:79], s[2:3], v[78:79] op_sel_hi:[0,1]
	v_rcp_f32_e32 v78, v78
	v_rcp_f32_e32 v79, v79
	s_nop 0
	v_pk_mul_f32 v[74:75], v[74:75], v[78:79]
	v_mov_b32_e32 v78, v35
	v_mov_b32_e32 v79, v35
	v_cvt_pk_fp8_f32 v78, v68, v69
	v_cvt_pk_fp8_f32 v79, v72, v73
	v_pk_mul_f32 v[74:75], v[76:77], v[74:75]
	v_add_u32_e32 v76, 0x90, v152
	v_cvt_pk_fp8_f32 v78, v70, v71 op_sel:[0,0,1]
	v_cvt_pk_fp8_f32 v79, v74, v75 op_sel:[0,0,1]
	v_ashrrev_i32_e32 v77, 31, v76
	v_lshlrev_b64 v[68:69], 10, v[76:77]
	v_lshl_add_u64 v[68:69], v[150:151], 0, v[68:69]
	global_store_dwordx2 v[68:69], v[78:79], off sc1
	v_pk_fma_f32 v[68:69], v[48:49], s[34:35], v[140:141] op_sel_hi:[1,0,1]
	v_pk_fma_f32 v[70:71], v[14:15], s[94:95], v[144:145] op_sel_hi:[1,0,1] clamp
	v_min_f32_e32 v68, v68, v34
	v_min_f32_e32 v69, v69, v34
	v_pk_mul_f32 v[72:73], s[30:31], v[68:69] op_sel_hi:[0,1]
	v_exp_f32_e32 v72, v72
	v_exp_f32_e32 v73, v73
	v_pk_fma_f32 v[70:71], s[0:1], v[70:71], s[0:1] op_sel:[0,0,1] op_sel_hi:[0,1,1]
	v_pk_add_f32 v[72:73], s[2:3], v[72:73] op_sel_hi:[0,1]
	v_rcp_f32_e32 v72, v72
	v_rcp_f32_e32 v73, v73
	s_nop 0
	v_pk_mul_f32 v[68:69], v[68:69], v[72:73]
	s_nop 0
	v_pk_mul_f32 v[68:69], v[70:71], v[68:69]
	v_pk_fma_f32 v[70:71], v[50:51], s[34:35], v[142:143] op_sel_hi:[1,0,1]
	v_pk_fma_f32 v[72:73], v[16:17], s[94:95], v[146:147] op_sel_hi:[1,0,1] clamp
	v_min_f32_e32 v70, v70, v34
	v_min_f32_e32 v71, v71, v34
	v_pk_mul_f32 v[74:75], s[30:31], v[70:71] op_sel_hi:[0,1]
	v_exp_f32_e32 v74, v74
	v_exp_f32_e32 v75, v75
	v_pk_fma_f32 v[72:73], s[0:1], v[72:73], s[0:1] op_sel:[0,0,1] op_sel_hi:[0,1,1]
	v_pk_add_f32 v[74:75], s[2:3], v[74:75] op_sel_hi:[0,1]
	v_rcp_f32_e32 v74, v74
	v_rcp_f32_e32 v75, v75
	s_nop 0
	v_pk_mul_f32 v[70:71], v[70:71], v[74:75]
	s_nop 0
	v_pk_mul_f32 v[70:71], v[72:73], v[70:71]
	v_pk_fma_f32 v[72:73], v[44:45], s[34:35], v[132:133] op_sel_hi:[1,0,1]
	v_pk_fma_f32 v[74:75], v[10:11], s[94:95], v[136:137] op_sel_hi:[1,0,1] clamp
	v_min_f32_e32 v72, v72, v34
	v_min_f32_e32 v73, v73, v34
	v_pk_mul_f32 v[76:77], s[30:31], v[72:73] op_sel_hi:[0,1]
	v_exp_f32_e32 v76, v76
	v_exp_f32_e32 v77, v77
	v_pk_fma_f32 v[74:75], s[0:1], v[74:75], s[0:1] op_sel:[0,0,1] op_sel_hi:[0,1,1]
	v_pk_add_f32 v[76:77], s[2:3], v[76:77] op_sel_hi:[0,1]
	v_rcp_f32_e32 v76, v76
	v_rcp_f32_e32 v77, v77
	s_nop 0
	v_pk_mul_f32 v[72:73], v[72:73], v[76:77]
	s_nop 0
	v_pk_mul_f32 v[72:73], v[74:75], v[72:73]
	v_pk_fma_f32 v[74:75], v[46:47], s[34:35], v[134:135] op_sel_hi:[1,0,1]
	v_pk_fma_f32 v[76:77], v[12:13], s[94:95], v[138:139] op_sel_hi:[1,0,1] clamp
	v_min_f32_e32 v74, v74, v34
	v_min_f32_e32 v75, v75, v34
	v_pk_mul_f32 v[78:79], s[30:31], v[74:75] op_sel_hi:[0,1]
	v_exp_f32_e32 v78, v78
	v_exp_f32_e32 v79, v79
	v_pk_fma_f32 v[76:77], s[0:1], v[76:77], s[0:1] op_sel:[0,0,1] op_sel_hi:[0,1,1]
	v_pk_add_f32 v[78:79], s[2:3], v[78:79] op_sel_hi:[0,1]
	v_rcp_f32_e32 v78, v78
	v_rcp_f32_e32 v79, v79
	s_nop 0
	v_pk_mul_f32 v[74:75], v[74:75], v[78:79]
	v_mov_b32_e32 v78, v35
	v_mov_b32_e32 v79, v35
	v_cvt_pk_fp8_f32 v78, v68, v69
	v_cvt_pk_fp8_f32 v79, v72, v73
	v_pk_mul_f32 v[74:75], v[76:77], v[74:75]
	v_add_u32_e32 v76, 0xa0, v152
	v_cvt_pk_fp8_f32 v78, v70, v71 op_sel:[0,0,1]
	v_cvt_pk_fp8_f32 v79, v74, v75 op_sel:[0,0,1]
	v_ashrrev_i32_e32 v77, 31, v76
	v_lshlrev_b64 v[68:69], 10, v[76:77]
	v_lshl_add_u64 v[68:69], v[150:151], 0, v[68:69]
	global_store_dwordx2 v[68:69], v[78:79], off sc1
	v_pk_fma_f32 v[68:69], v[6:7], s[34:35], v[140:141] op_sel_hi:[1,0,1]
	v_pk_fma_f32 v[70:71], v[92:93], s[94:95], v[144:145] op_sel_hi:[1,0,1] clamp
	v_min_f32_e32 v68, v68, v34
	v_min_f32_e32 v69, v69, v34
	v_pk_mul_f32 v[72:73], s[30:31], v[68:69] op_sel_hi:[0,1]
	v_exp_f32_e32 v72, v72
	v_exp_f32_e32 v73, v73
	v_pk_fma_f32 v[70:71], s[0:1], v[70:71], s[0:1] op_sel:[0,0,1] op_sel_hi:[0,1,1]
	v_pk_add_f32 v[72:73], s[2:3], v[72:73] op_sel_hi:[0,1]
	v_rcp_f32_e32 v72, v72
	v_rcp_f32_e32 v73, v73
	s_nop 0
	v_pk_mul_f32 v[68:69], v[68:69], v[72:73]
	s_nop 0
	v_pk_mul_f32 v[68:69], v[70:71], v[68:69]
	v_pk_fma_f32 v[70:71], v[8:9], s[34:35], v[142:143] op_sel_hi:[1,0,1]
	v_pk_fma_f32 v[72:73], v[94:95], s[94:95], v[146:147] op_sel_hi:[1,0,1] clamp
	v_min_f32_e32 v70, v70, v34
	v_min_f32_e32 v71, v71, v34
	v_pk_mul_f32 v[74:75], s[30:31], v[70:71] op_sel_hi:[0,1]
	v_exp_f32_e32 v74, v74
	v_exp_f32_e32 v75, v75
	v_pk_fma_f32 v[72:73], s[0:1], v[72:73], s[0:1] op_sel:[0,0,1] op_sel_hi:[0,1,1]
	v_pk_add_f32 v[74:75], s[2:3], v[74:75] op_sel_hi:[0,1]
	v_rcp_f32_e32 v74, v74
	v_rcp_f32_e32 v75, v75
	s_nop 0
	v_pk_mul_f32 v[70:71], v[70:71], v[74:75]
	s_nop 0
	v_pk_mul_f32 v[70:71], v[72:73], v[70:71]
	v_pk_fma_f32 v[72:73], v[244:245], s[34:35], v[132:133] op_sel_hi:[1,0,1]
	v_pk_fma_f32 v[74:75], v[2:3], s[94:95], v[136:137] op_sel_hi:[1,0,1] clamp
	v_min_f32_e32 v72, v72, v34
	v_min_f32_e32 v73, v73, v34
	v_pk_mul_f32 v[76:77], s[30:31], v[72:73] op_sel_hi:[0,1]
	v_exp_f32_e32 v76, v76
	v_exp_f32_e32 v77, v77
	v_pk_fma_f32 v[74:75], s[0:1], v[74:75], s[0:1] op_sel:[0,0,1] op_sel_hi:[0,1,1]
	v_pk_add_f32 v[76:77], s[2:3], v[76:77] op_sel_hi:[0,1]
	v_rcp_f32_e32 v76, v76
	v_rcp_f32_e32 v77, v77
	s_nop 0
	v_pk_mul_f32 v[72:73], v[72:73], v[76:77]
	s_nop 0
	v_pk_mul_f32 v[72:73], v[74:75], v[72:73]
	v_pk_fma_f32 v[74:75], v[246:247], s[34:35], v[134:135] op_sel_hi:[1,0,1]
	v_pk_fma_f32 v[76:77], v[4:5], s[94:95], v[138:139] op_sel_hi:[1,0,1] clamp
	v_min_f32_e32 v74, v74, v34
	v_min_f32_e32 v75, v75, v34
	v_pk_mul_f32 v[78:79], s[30:31], v[74:75] op_sel_hi:[0,1]
	v_exp_f32_e32 v78, v78
	v_exp_f32_e32 v79, v79
	v_pk_fma_f32 v[76:77], s[0:1], v[76:77], s[0:1] op_sel:[0,0,1] op_sel_hi:[0,1,1]
	v_pk_add_f32 v[78:79], s[2:3], v[78:79] op_sel_hi:[0,1]
	v_rcp_f32_e32 v78, v78
	v_rcp_f32_e32 v79, v79
	s_nop 0
	v_pk_mul_f32 v[74:75], v[74:75], v[78:79]
	v_mov_b32_e32 v78, v35
	v_mov_b32_e32 v79, v35
	v_cvt_pk_fp8_f32 v78, v68, v69
	v_cvt_pk_fp8_f32 v79, v72, v73
	v_pk_mul_f32 v[74:75], v[76:77], v[74:75]
	v_add_u32_e32 v76, 0xb0, v152
	v_cvt_pk_fp8_f32 v78, v70, v71 op_sel:[0,0,1]
	v_cvt_pk_fp8_f32 v79, v74, v75 op_sel:[0,0,1]
	v_ashrrev_i32_e32 v77, 31, v76
	v_lshlrev_b64 v[68:69], 10, v[76:77]
	v_lshl_add_u64 v[68:69], v[150:151], 0, v[68:69]
	global_store_dwordx2 v[68:69], v[78:79], off sc1
	s_cbranch_vccnz .LBB0_1371
; template <class Epi, class Src>
; __device__ __forceinline__ void gemm_phase(LAS unsigned char* lds, const Src S, const Epi E) {
;     ...
;         if (!has_next) break;
; #pragma unroll
;         for (int a = 0; a < 2; ++a)
; #pragma unroll
;             for (int b = 0; b < 2; ++b)
; #pragma unroll
;                 for (int m = 0; m < 4; ++m)
; #pragma unroll
;                     for (int n = 0; n < 2; ++n) acc[a][b][m][n] = (f32x4){0.f, 0.f, 0.f, 0.f};
;         cur = nxt; cB = nB; cA = nA; ++ui; par ^= 1;
	s_mov_b32 s39, s71
	s_mov_b32 s18, s26
	s_mov_b32 s38, s70
	s_mov_b32 s16, s22
	s_mov_b32 s68, s3
	s_mov_b64 s[20:21], s[28:29]
	s_mov_b32 s57, s72
	s_xor_b64 s[0:1], s[24:25], -1
	s_andn2_b64 vcc, exec, s[0:1]
	s_cbranch_vccnz .LBB0_1372
	s_branch .LBB0_1373
